# epilogue load hoisting for P16 (EpiResidN bf16 base) and q-GEMM SSP loads (P5,P17)
# speedup vs baseline: 1.0010x; 1.0010x over previous
.LBB0_855:
	s_add_u32 s4, s48, 0x18600000
	s_addc_u32 s5, s49, 0
	s_lshl_b32 s6, s20, 8
	s_add_i32 s22, s22, s6
	s_lshl_b32 s7, s19, 8
	v_add_u32_e32 v132, s22, v139
	v_ashrrev_i32_e32 v133, 31, v132
	v_lshlrev_b64 v[134:135], 6, v[132:133]
	v_lshl_add_u64 v[134:135], s[4:5], 0, v[134:135]
	global_load_dwordx4 v[140:143], v[134:135], off
	global_load_dwordx4 v[144:147], v[134:135], off offset:32
	global_load_dwordx4 v[148:151], v[134:135], off offset:16
	global_load_dwordx4 v[152:155], v[134:135], off offset:48
	v_mov_b32_e32 v240, v134
	v_mov_b32_e32 v241, v135
	v_add_co_u32_e32 v242, vcc, 0x400, v240
	s_nop 1
	v_addc_co_u32_e32 v243, vcc, 0, v241, vcc
	global_load_dwordx4 v[160:163], v[242:243], off
	global_load_dwordx4 v[164:167], v[242:243], off offset:32
	global_load_dwordx4 v[168:171], v[242:243], off offset:16
	global_load_dwordx4 v[172:175], v[242:243], off offset:48
	v_add_co_u32_e32 v242, vcc, 0x800, v240
	s_nop 1
	v_addc_co_u32_e32 v243, vcc, 0, v241, vcc
	global_load_dwordx4 v[176:179], v[242:243], off
	global_load_dwordx4 v[180:183], v[242:243], off offset:32
	global_load_dwordx4 v[184:187], v[242:243], off offset:16
	global_load_dwordx4 v[188:191], v[242:243], off offset:48
	v_add_co_u32_e32 v242, vcc, 0xc00, v240
	s_nop 1
	v_addc_co_u32_e32 v243, vcc, 0, v241, vcc
	global_load_dwordx4 v[192:195], v[242:243], off
	global_load_dwordx4 v[196:199], v[242:243], off offset:32
	global_load_dwordx4 v[200:203], v[242:243], off offset:16
	global_load_dwordx4 v[204:207], v[242:243], off offset:48
	v_add_co_u32_e32 v242, vcc, 0x2000, v240
	s_nop 1
	v_addc_co_u32_e32 v243, vcc, 0, v241, vcc
	global_load_dwordx4 v[208:211], v[242:243], off
	global_load_dwordx4 v[212:215], v[242:243], off offset:32
	global_load_dwordx4 v[216:219], v[242:243], off offset:16
	global_load_dwordx4 v[220:223], v[242:243], off offset:48
	v_add_co_u32_e32 v242, vcc, 0x2400, v240
	s_nop 1
	v_addc_co_u32_e32 v243, vcc, 0, v241, vcc
	global_load_dwordx4 v[224:227], v[242:243], off
	global_load_dwordx4 v[228:231], v[242:243], off offset:32
	global_load_dwordx4 v[232:235], v[242:243], off offset:16
	global_load_dwordx4 v[236:239], v[242:243], off offset:48
	s_or_b32 s7, s21, s7
	v_mov_b32_e32 v134, 0x358637bd
	v_lshl_add_u32 v130, v1, 3, s7
	s_mov_b32 s6, 0x800000
	v_lshlrev_b64 v[156:157], 11, v[132:133]
	v_mov_b32_e32 v129, v131
	v_ashrrev_i32_e32 v131, 31, v130
	v_add_u32_e32 v136, 16, v132
	v_lshlrev_b64 v[130:131], 1, v[130:131]
	v_ashrrev_i32_e32 v137, 31, v136
	v_lshl_add_u64 v[156:157], s[46:47], 0, v[156:157]
	s_cmpk_lt_u32 s18, 0x100
	s_waitcnt vmcnt(20)
	v_mov_b32_e32 v158, v140
	v_mov_b32_e32 v159, v144
	v_mov_b32_e32 v144, v141
	v_mov_b32_e32 v140, v142
	v_mov_b32_e32 v141, v146
	v_mov_b32_e32 v146, v143
	v_mov_b32_e32 v142, v148
	v_mov_b32_e32 v143, v152
	v_mov_b32_e32 v152, v149
	v_mov_b32_e32 v148, v150
	v_mov_b32_e32 v149, v154
	v_mov_b32_e32 v154, v151
	v_pk_add_f32 v[144:145], v[158:159], v[144:145]
	v_pk_add_f32 v[140:141], v[140:141], v[146:147]
	v_pk_add_f32 v[142:143], v[142:143], v[152:153]
	v_pk_add_f32 v[146:147], v[148:149], v[154:155]
	v_pk_add_f32 v[140:141], v[144:145], v[140:141]
	v_pk_add_f32 v[142:143], v[142:143], v[146:147]
	s_nop 0
	v_pk_add_f32 v[140:141], v[140:141], v[142:143]
	v_lshl_add_u64 v[142:143], v[156:157], 0, v[130:131]
	v_add_f32_e32 v1, v140, v141
	v_fmamk_f32 v1, v1, 0x3a800000, v134
	v_mul_f32_e32 v133, 0x4b800000, v1
	v_cmp_gt_f32_e32 vcc, s6, v1
	v_lshlrev_b64 v[140:141], 6, v[136:137]
	v_lshl_add_u64 v[140:141], s[4:5], 0, v[140:141]
	v_cndmask_b32_e32 v1, v1, v133, vcc
	v_rsq_f32_e32 v1, v1
	v_lshlrev_b64 v[136:137], 11, v[136:137]
	v_mul_f32_e32 v133, 0x45800000, v1
	v_cndmask_b32_e32 v144, v1, v133, vcc
	v_pk_mul_f32 v[128:129], v[128:129], v[144:145] op_sel_hi:[1,0]
	v_pk_mul_f32 v[126:127], v[126:127], v[144:145] op_sel_hi:[1,0]
	v_pk_mul_f32 v[124:125], v[124:125], v[144:145] op_sel_hi:[1,0]
	v_pk_mul_f32 v[122:123], v[122:123], v[144:145] op_sel_hi:[1,0]
	v_pk_mul_f32 v[120:121], v[120:121], v[144:145] op_sel_hi:[1,0]
	v_pk_mul_f32 v[118:119], v[118:119], v[144:145] op_sel_hi:[1,0]
	v_pk_mul_f32 v[146:147], v[116:117], v[144:145] op_sel_hi:[1,0]
	v_pk_mul_f32 v[144:145], v[114:115], v[144:145] op_sel_hi:[1,0]
	v_cvt_pk_bf16_f32 v114, v126, v127
	v_cvt_pk_bf16_f32 v115, v128, v129
	v_cvt_pk_bf16_f32 v116, v122, v123
	v_cvt_pk_bf16_f32 v117, v124, v125
	v_cvt_pk_bf16_f32 v118, v118, v119
	v_cvt_pk_bf16_f32 v119, v120, v121
	v_cvt_pk_bf16_f32 v120, v144, v145
	v_cvt_pk_bf16_f32 v121, v146, v147
	global_store_dwordx4 v[142:143], v[114:117], off
	global_store_dwordx4 v[142:143], v[118:121], off offset:256
	s_nop 0
	v_add_u32_e32 v140, 32, v132
	v_ashrrev_i32_e32 v141, 31, v140
	v_lshlrev_b64 v[142:143], 6, v[140:141]
	s_waitcnt vmcnt(18)
	v_mov_b32_e32 v114, v160
	v_mov_b32_e32 v115, v161
	v_mov_b32_e32 v116, v162
	v_mov_b32_e32 v117, v163
	v_mov_b32_e32 v118, v164
	v_mov_b32_e32 v119, v165
	v_mov_b32_e32 v120, v166
	v_mov_b32_e32 v121, v167
	v_mov_b32_e32 v122, v168
	v_mov_b32_e32 v123, v169
	v_mov_b32_e32 v124, v170
	v_mov_b32_e32 v125, v171
	v_mov_b32_e32 v126, v172
	v_mov_b32_e32 v127, v173
	v_mov_b32_e32 v128, v174
	v_mov_b32_e32 v129, v175
	v_add_co_u32_e32 v242, vcc, 0x2800, v240
	s_nop 1
	v_addc_co_u32_e32 v243, vcc, 0, v241, vcc
	global_load_dwordx4 v[160:163], v[242:243], off
	global_load_dwordx4 v[164:167], v[242:243], off offset:32
	global_load_dwordx4 v[168:171], v[242:243], off offset:16
	global_load_dwordx4 v[172:175], v[242:243], off offset:48
	v_mov_b32_e32 v144, v114
	v_mov_b32_e32 v145, v118
	v_mov_b32_e32 v118, v115
	v_mov_b32_e32 v114, v116
	v_mov_b32_e32 v115, v120
	v_mov_b32_e32 v120, v117
	v_mov_b32_e32 v116, v122
	v_mov_b32_e32 v117, v126
	v_mov_b32_e32 v126, v123
	v_mov_b32_e32 v122, v124
	v_mov_b32_e32 v123, v128
	v_mov_b32_e32 v128, v125
	v_pk_add_f32 v[118:119], v[144:145], v[118:119]
	v_pk_add_f32 v[114:115], v[114:115], v[120:121]
	v_pk_add_f32 v[116:117], v[116:117], v[126:127]
	v_pk_add_f32 v[120:121], v[122:123], v[128:129]
	v_pk_add_f32 v[114:115], v[118:119], v[114:115]
	v_pk_add_f32 v[116:117], v[116:117], v[120:121]
	s_nop 0
	v_pk_add_f32 v[114:115], v[114:115], v[116:117]
	v_lshl_add_u64 v[116:117], s[4:5], 0, v[142:143]
	v_add_f32_e32 v1, v114, v115
	v_fmamk_f32 v1, v1, 0x3a800000, v134
	v_mul_f32_e32 v114, 0x4b800000, v1
	v_cmp_gt_f32_e32 vcc, s6, v1
	s_nop 1
	v_cndmask_b32_e32 v1, v1, v114, vcc
	v_rsq_f32_e32 v1, v1
	v_lshl_add_u64 v[114:115], s[46:47], 0, v[136:137]
	v_lshl_add_u64 v[114:115], v[114:115], 0, v[130:131]
	v_mul_f32_e32 v118, 0x45800000, v1
	v_cndmask_b32_e32 v118, v1, v118, vcc
	v_pk_mul_f32 v[112:113], v[112:113], v[118:119] op_sel_hi:[1,0]
	v_pk_mul_f32 v[110:111], v[110:111], v[118:119] op_sel_hi:[1,0]
	v_pk_mul_f32 v[108:109], v[108:109], v[118:119] op_sel_hi:[1,0]
	v_pk_mul_f32 v[106:107], v[106:107], v[118:119] op_sel_hi:[1,0]
	v_pk_mul_f32 v[104:105], v[104:105], v[118:119] op_sel_hi:[1,0]
	v_pk_mul_f32 v[102:103], v[102:103], v[118:119] op_sel_hi:[1,0]
	v_pk_mul_f32 v[120:121], v[100:101], v[118:119] op_sel_hi:[1,0]
	v_pk_mul_f32 v[118:119], v[98:99], v[118:119] op_sel_hi:[1,0]
	v_cvt_pk_bf16_f32 v98, v110, v111
	v_cvt_pk_bf16_f32 v99, v112, v113
	v_cvt_pk_bf16_f32 v100, v106, v107
	v_cvt_pk_bf16_f32 v101, v108, v109
	v_cvt_pk_bf16_f32 v102, v102, v103
	v_cvt_pk_bf16_f32 v103, v104, v105
	v_cvt_pk_bf16_f32 v104, v118, v119
	v_cvt_pk_bf16_f32 v105, v120, v121
	global_store_dwordx4 v[114:115], v[98:101], off
	global_store_dwordx4 v[114:115], v[102:105], off offset:256
	s_nop 0
	v_add_u32_e32 v114, 48, v132
	v_lshlrev_b64 v[116:117], 11, v[140:141]
	v_ashrrev_i32_e32 v115, 31, v114
	v_lshlrev_b64 v[118:119], 6, v[114:115]
	s_waitcnt vmcnt(20)
	v_mov_b32_e32 v98, v176
	v_mov_b32_e32 v99, v177
	v_mov_b32_e32 v100, v178
	v_mov_b32_e32 v101, v179
	v_mov_b32_e32 v102, v180
	v_mov_b32_e32 v103, v181
	v_mov_b32_e32 v104, v182
	v_mov_b32_e32 v105, v183
	v_mov_b32_e32 v106, v184
	v_mov_b32_e32 v107, v185
	v_mov_b32_e32 v108, v186
	v_mov_b32_e32 v109, v187
	v_mov_b32_e32 v110, v188
	v_mov_b32_e32 v111, v189
	v_mov_b32_e32 v112, v190
	v_mov_b32_e32 v113, v191
	v_add_co_u32_e32 v242, vcc, 0x2c00, v240
	s_nop 1
	v_addc_co_u32_e32 v243, vcc, 0, v241, vcc
	global_load_dwordx4 v[176:179], v[242:243], off
	global_load_dwordx4 v[180:183], v[242:243], off offset:32
	global_load_dwordx4 v[184:187], v[242:243], off offset:16
	global_load_dwordx4 v[188:191], v[242:243], off offset:48
	v_mov_b32_e32 v120, v98
	v_mov_b32_e32 v121, v102
	v_mov_b32_e32 v102, v99
	v_mov_b32_e32 v98, v100
	v_mov_b32_e32 v99, v104
	v_mov_b32_e32 v104, v101
	v_mov_b32_e32 v100, v106
	v_mov_b32_e32 v101, v110
	v_mov_b32_e32 v110, v107
	v_mov_b32_e32 v106, v108
	v_mov_b32_e32 v107, v112
	v_mov_b32_e32 v112, v109
	v_pk_add_f32 v[102:103], v[120:121], v[102:103]
	v_pk_add_f32 v[98:99], v[98:99], v[104:105]
	v_pk_add_f32 v[100:101], v[100:101], v[110:111]
	v_pk_add_f32 v[104:105], v[106:107], v[112:113]
	v_pk_add_f32 v[98:99], v[102:103], v[98:99]
	v_pk_add_f32 v[100:101], v[100:101], v[104:105]
	s_nop 0
	v_pk_add_f32 v[98:99], v[98:99], v[100:101]
	v_lshl_add_u64 v[100:101], s[4:5], 0, v[118:119]
	v_add_f32_e32 v1, v98, v99
	v_fmamk_f32 v1, v1, 0x3a800000, v134
	v_mul_f32_e32 v98, 0x4b800000, v1
	v_cmp_gt_f32_e32 vcc, s6, v1
	s_nop 1
	v_cndmask_b32_e32 v1, v1, v98, vcc
	v_rsq_f32_e32 v1, v1
	v_lshl_add_u64 v[98:99], s[46:47], 0, v[116:117]
	v_lshl_add_u64 v[98:99], v[98:99], 0, v[130:131]
	v_mul_f32_e32 v102, 0x45800000, v1
	v_cndmask_b32_e32 v102, v1, v102, vcc
	v_pk_mul_f32 v[96:97], v[96:97], v[102:103] op_sel_hi:[1,0]
	v_pk_mul_f32 v[94:95], v[94:95], v[102:103] op_sel_hi:[1,0]
	v_pk_mul_f32 v[92:93], v[92:93], v[102:103] op_sel_hi:[1,0]
	v_pk_mul_f32 v[90:91], v[90:91], v[102:103] op_sel_hi:[1,0]
	v_pk_mul_f32 v[88:89], v[88:89], v[102:103] op_sel_hi:[1,0]
	v_pk_mul_f32 v[86:87], v[86:87], v[102:103] op_sel_hi:[1,0]
	v_pk_mul_f32 v[104:105], v[84:85], v[102:103] op_sel_hi:[1,0]
	v_pk_mul_f32 v[102:103], v[82:83], v[102:103] op_sel_hi:[1,0]
	v_cvt_pk_bf16_f32 v82, v94, v95
	v_cvt_pk_bf16_f32 v83, v96, v97
	v_cvt_pk_bf16_f32 v84, v90, v91
	v_cvt_pk_bf16_f32 v85, v92, v93
	v_cvt_pk_bf16_f32 v86, v86, v87
	v_cvt_pk_bf16_f32 v87, v88, v89
	v_cvt_pk_bf16_f32 v88, v102, v103
	v_cvt_pk_bf16_f32 v89, v104, v105
	global_store_dwordx4 v[98:99], v[82:85], off
	global_store_dwordx4 v[98:99], v[86:89], off offset:256
	s_nop 0
	v_add_u32_e32 v98, 0x80, v132
	v_lshlrev_b64 v[100:101], 11, v[114:115]
	v_ashrrev_i32_e32 v99, 31, v98
	v_lshlrev_b64 v[102:103], 6, v[98:99]
	s_waitcnt vmcnt(22)
	v_mov_b32_e32 v82, v192
	v_mov_b32_e32 v83, v193
	v_mov_b32_e32 v84, v194
	v_mov_b32_e32 v85, v195
	v_mov_b32_e32 v86, v196
	v_mov_b32_e32 v87, v197
	v_mov_b32_e32 v88, v198
	v_mov_b32_e32 v89, v199
	v_mov_b32_e32 v90, v200
	v_mov_b32_e32 v91, v201
	v_mov_b32_e32 v92, v202
	v_mov_b32_e32 v93, v203
	v_mov_b32_e32 v94, v204
	v_mov_b32_e32 v95, v205
	v_mov_b32_e32 v96, v206
	v_mov_b32_e32 v97, v207
	v_mov_b32_e32 v104, v82
	v_mov_b32_e32 v105, v86
	v_mov_b32_e32 v86, v83
	v_mov_b32_e32 v82, v84
	v_mov_b32_e32 v83, v88
	v_mov_b32_e32 v88, v85
	v_mov_b32_e32 v84, v90
	v_mov_b32_e32 v85, v94
	v_mov_b32_e32 v94, v91
	v_mov_b32_e32 v90, v92
	v_mov_b32_e32 v91, v96
	v_mov_b32_e32 v96, v93
	v_pk_add_f32 v[86:87], v[104:105], v[86:87]
	v_pk_add_f32 v[82:83], v[82:83], v[88:89]
	v_pk_add_f32 v[84:85], v[84:85], v[94:95]
	v_pk_add_f32 v[88:89], v[90:91], v[96:97]
	v_pk_add_f32 v[82:83], v[86:87], v[82:83]
	v_pk_add_f32 v[84:85], v[84:85], v[88:89]
	s_nop 0
	v_pk_add_f32 v[82:83], v[82:83], v[84:85]
	v_lshl_add_u64 v[84:85], s[4:5], 0, v[102:103]
	v_add_f32_e32 v1, v82, v83
	v_fmamk_f32 v1, v1, 0x3a800000, v134
	v_mul_f32_e32 v82, 0x4b800000, v1
	v_cmp_gt_f32_e32 vcc, s6, v1
	s_nop 1
	v_cndmask_b32_e32 v1, v1, v82, vcc
	v_rsq_f32_e32 v1, v1
	v_lshl_add_u64 v[82:83], s[46:47], 0, v[100:101]
	v_lshl_add_u64 v[82:83], v[82:83], 0, v[130:131]
	v_mul_f32_e32 v86, 0x45800000, v1
	v_cndmask_b32_e32 v86, v1, v86, vcc
	v_pk_mul_f32 v[80:81], v[80:81], v[86:87] op_sel_hi:[1,0]
	v_pk_mul_f32 v[78:79], v[78:79], v[86:87] op_sel_hi:[1,0]
	v_pk_mul_f32 v[76:77], v[76:77], v[86:87] op_sel_hi:[1,0]
	v_pk_mul_f32 v[74:75], v[74:75], v[86:87] op_sel_hi:[1,0]
	v_pk_mul_f32 v[72:73], v[72:73], v[86:87] op_sel_hi:[1,0]
	v_pk_mul_f32 v[70:71], v[70:71], v[86:87] op_sel_hi:[1,0]
	v_pk_mul_f32 v[88:89], v[68:69], v[86:87] op_sel_hi:[1,0]
	v_pk_mul_f32 v[86:87], v[66:67], v[86:87] op_sel_hi:[1,0]
	v_cvt_pk_bf16_f32 v66, v78, v79
	v_cvt_pk_bf16_f32 v67, v80, v81
	v_cvt_pk_bf16_f32 v68, v74, v75
	v_cvt_pk_bf16_f32 v69, v76, v77
	v_cvt_pk_bf16_f32 v70, v70, v71
	v_cvt_pk_bf16_f32 v71, v72, v73
	v_cvt_pk_bf16_f32 v72, v86, v87
	v_cvt_pk_bf16_f32 v73, v88, v89
	global_store_dwordx4 v[82:83], v[66:69], off
	global_store_dwordx4 v[82:83], v[70:73], off offset:256
	s_nop 0
	v_add_u32_e32 v82, 0x90, v132
	v_lshlrev_b64 v[84:85], 11, v[98:99]
	v_ashrrev_i32_e32 v83, 31, v82
	v_lshlrev_b64 v[86:87], 6, v[82:83]
	s_waitcnt vmcnt(20)
	v_mov_b32_e32 v66, v208
	v_mov_b32_e32 v67, v209
	v_mov_b32_e32 v68, v210
	v_mov_b32_e32 v69, v211
	v_mov_b32_e32 v70, v212
	v_mov_b32_e32 v71, v213
	v_mov_b32_e32 v72, v214
	v_mov_b32_e32 v73, v215
	v_mov_b32_e32 v74, v216
	v_mov_b32_e32 v75, v217
	v_mov_b32_e32 v76, v218
	v_mov_b32_e32 v77, v219
	v_mov_b32_e32 v78, v220
	v_mov_b32_e32 v79, v221
	v_mov_b32_e32 v80, v222
	v_mov_b32_e32 v81, v223
	v_mov_b32_e32 v88, v66
	v_mov_b32_e32 v89, v70
	v_mov_b32_e32 v70, v67
	v_mov_b32_e32 v66, v68
	v_mov_b32_e32 v67, v72
	v_mov_b32_e32 v72, v69
	v_mov_b32_e32 v68, v74
	v_mov_b32_e32 v69, v78
	v_mov_b32_e32 v78, v75
	v_mov_b32_e32 v74, v76
	v_mov_b32_e32 v75, v80
	v_mov_b32_e32 v80, v77
	v_pk_add_f32 v[70:71], v[88:89], v[70:71]
	v_pk_add_f32 v[66:67], v[66:67], v[72:73]
	v_pk_add_f32 v[68:69], v[68:69], v[78:79]
	v_pk_add_f32 v[72:73], v[74:75], v[80:81]
	v_pk_add_f32 v[66:67], v[70:71], v[66:67]
	v_pk_add_f32 v[68:69], v[68:69], v[72:73]
	s_nop 0
	v_pk_add_f32 v[66:67], v[66:67], v[68:69]
	v_lshl_add_u64 v[68:69], s[4:5], 0, v[86:87]
	v_add_f32_e32 v1, v66, v67
	v_fmamk_f32 v1, v1, 0x3a800000, v134
	v_mul_f32_e32 v66, 0x4b800000, v1
	v_cmp_gt_f32_e32 vcc, s6, v1
	s_nop 1
	v_cndmask_b32_e32 v1, v1, v66, vcc
	v_rsq_f32_e32 v1, v1
	v_lshl_add_u64 v[66:67], s[46:47], 0, v[84:85]
	v_lshl_add_u64 v[66:67], v[66:67], 0, v[130:131]
	v_mul_f32_e32 v70, 0x45800000, v1
	v_cndmask_b32_e32 v70, v1, v70, vcc
	v_pk_mul_f32 v[64:65], v[64:65], v[70:71] op_sel_hi:[1,0]
	v_pk_mul_f32 v[62:63], v[62:63], v[70:71] op_sel_hi:[1,0]
	v_pk_mul_f32 v[60:61], v[60:61], v[70:71] op_sel_hi:[1,0]
	v_pk_mul_f32 v[58:59], v[58:59], v[70:71] op_sel_hi:[1,0]
	v_pk_mul_f32 v[56:57], v[56:57], v[70:71] op_sel_hi:[1,0]
	v_pk_mul_f32 v[54:55], v[54:55], v[70:71] op_sel_hi:[1,0]
	v_pk_mul_f32 v[72:73], v[52:53], v[70:71] op_sel_hi:[1,0]
	v_pk_mul_f32 v[70:71], v[50:51], v[70:71] op_sel_hi:[1,0]
	v_cvt_pk_bf16_f32 v50, v62, v63
	v_cvt_pk_bf16_f32 v51, v64, v65
	v_cvt_pk_bf16_f32 v52, v58, v59
	v_cvt_pk_bf16_f32 v53, v60, v61
	v_cvt_pk_bf16_f32 v54, v54, v55
	v_cvt_pk_bf16_f32 v55, v56, v57
	v_cvt_pk_bf16_f32 v56, v70, v71
	v_cvt_pk_bf16_f32 v57, v72, v73
	global_store_dwordx4 v[66:67], v[50:53], off
	global_store_dwordx4 v[66:67], v[54:57], off offset:256
	s_nop 0
	v_add_u32_e32 v66, 0xa0, v132
	v_lshlrev_b64 v[68:69], 11, v[82:83]
	v_ashrrev_i32_e32 v67, 31, v66
	v_lshlrev_b64 v[70:71], 6, v[66:67]
	s_waitcnt vmcnt(18)
	v_mov_b32_e32 v50, v224
	v_mov_b32_e32 v51, v225
	v_mov_b32_e32 v52, v226
	v_mov_b32_e32 v53, v227
	v_mov_b32_e32 v54, v228
	v_mov_b32_e32 v55, v229
	v_mov_b32_e32 v56, v230
	v_mov_b32_e32 v57, v231
	v_mov_b32_e32 v58, v232
	v_mov_b32_e32 v59, v233
	v_mov_b32_e32 v60, v234
	v_mov_b32_e32 v61, v235
	v_mov_b32_e32 v62, v236
	v_mov_b32_e32 v63, v237
	v_mov_b32_e32 v64, v238
	v_mov_b32_e32 v65, v239
	v_mov_b32_e32 v72, v50
	v_mov_b32_e32 v73, v54
	v_mov_b32_e32 v54, v51
	v_mov_b32_e32 v50, v52
	v_mov_b32_e32 v51, v56
	v_mov_b32_e32 v56, v53
	v_mov_b32_e32 v52, v58
	v_mov_b32_e32 v53, v62
	v_mov_b32_e32 v62, v59
	v_mov_b32_e32 v58, v60
	v_mov_b32_e32 v59, v64
	v_mov_b32_e32 v64, v61
	v_pk_add_f32 v[54:55], v[72:73], v[54:55]
	v_pk_add_f32 v[50:51], v[50:51], v[56:57]
	v_pk_add_f32 v[52:53], v[52:53], v[62:63]
	v_pk_add_f32 v[56:57], v[58:59], v[64:65]
	v_pk_add_f32 v[50:51], v[54:55], v[50:51]
	v_pk_add_f32 v[52:53], v[52:53], v[56:57]
	s_nop 0
	v_pk_add_f32 v[50:51], v[50:51], v[52:53]
	v_lshl_add_u64 v[52:53], s[4:5], 0, v[70:71]
	v_add_f32_e32 v1, v50, v51
	v_fmamk_f32 v1, v1, 0x3a800000, v134
	v_mul_f32_e32 v50, 0x4b800000, v1
	v_cmp_gt_f32_e32 vcc, s6, v1
	s_nop 1
	v_cndmask_b32_e32 v1, v1, v50, vcc
	v_rsq_f32_e32 v1, v1
	v_lshl_add_u64 v[50:51], s[46:47], 0, v[68:69]
	v_lshl_add_u64 v[50:51], v[50:51], 0, v[130:131]
	v_mul_f32_e32 v54, 0x45800000, v1
	v_cndmask_b32_e32 v54, v1, v54, vcc
	v_pk_mul_f32 v[48:49], v[48:49], v[54:55] op_sel_hi:[1,0]
	v_pk_mul_f32 v[46:47], v[46:47], v[54:55] op_sel_hi:[1,0]
	v_pk_mul_f32 v[44:45], v[44:45], v[54:55] op_sel_hi:[1,0]
	v_pk_mul_f32 v[42:43], v[42:43], v[54:55] op_sel_hi:[1,0]
	v_pk_mul_f32 v[40:41], v[40:41], v[54:55] op_sel_hi:[1,0]
	v_pk_mul_f32 v[38:39], v[38:39], v[54:55] op_sel_hi:[1,0]
	v_pk_mul_f32 v[56:57], v[36:37], v[54:55] op_sel_hi:[1,0]
	v_pk_mul_f32 v[54:55], v[34:35], v[54:55] op_sel_hi:[1,0]
	v_cvt_pk_bf16_f32 v34, v46, v47
	v_cvt_pk_bf16_f32 v35, v48, v49
	v_cvt_pk_bf16_f32 v36, v42, v43
	v_cvt_pk_bf16_f32 v37, v44, v45
	v_cvt_pk_bf16_f32 v38, v38, v39
	v_cvt_pk_bf16_f32 v39, v40, v41
	v_cvt_pk_bf16_f32 v40, v54, v55
	v_cvt_pk_bf16_f32 v41, v56, v57
	global_store_dwordx4 v[50:51], v[34:37], off
	global_store_dwordx4 v[50:51], v[38:41], off offset:256
	s_nop 0
	v_add_u32_e32 v50, 0xb0, v132
	v_lshlrev_b64 v[52:53], 11, v[66:67]
	v_ashrrev_i32_e32 v51, 31, v50
	v_lshlrev_b64 v[54:55], 6, v[50:51]
	s_waitcnt vmcnt(14)
	v_mov_b32_e32 v34, v160
	v_mov_b32_e32 v35, v161
	v_mov_b32_e32 v36, v162
	v_mov_b32_e32 v37, v163
	v_mov_b32_e32 v38, v164
	v_mov_b32_e32 v39, v165
	v_mov_b32_e32 v40, v166
	v_mov_b32_e32 v41, v167
	v_mov_b32_e32 v42, v168
	v_mov_b32_e32 v43, v169
	v_mov_b32_e32 v44, v170
	v_mov_b32_e32 v45, v171
	v_mov_b32_e32 v46, v172
	v_mov_b32_e32 v47, v173
	v_mov_b32_e32 v48, v174
	v_mov_b32_e32 v49, v175
	v_mov_b32_e32 v56, v34
	v_mov_b32_e32 v57, v38
	v_mov_b32_e32 v38, v35
	v_mov_b32_e32 v34, v36
	v_mov_b32_e32 v35, v40
	v_mov_b32_e32 v40, v37
	v_mov_b32_e32 v36, v42
	v_mov_b32_e32 v37, v46
	v_mov_b32_e32 v46, v43
	v_mov_b32_e32 v42, v44
	v_mov_b32_e32 v43, v48
	v_mov_b32_e32 v48, v45
	v_pk_add_f32 v[38:39], v[56:57], v[38:39]
	v_pk_add_f32 v[34:35], v[34:35], v[40:41]
	v_pk_add_f32 v[36:37], v[36:37], v[46:47]
	v_pk_add_f32 v[40:41], v[42:43], v[48:49]
	v_pk_add_f32 v[34:35], v[38:39], v[34:35]
	v_pk_add_f32 v[36:37], v[36:37], v[40:41]
	s_nop 0
	v_pk_add_f32 v[34:35], v[34:35], v[36:37]
	v_lshl_add_u64 v[36:37], s[4:5], 0, v[54:55]
	v_add_f32_e32 v1, v34, v35
	v_fmamk_f32 v1, v1, 0x3a800000, v134
	v_mul_f32_e32 v34, 0x4b800000, v1
	v_cmp_gt_f32_e32 vcc, s6, v1
	s_nop 1
	v_cndmask_b32_e32 v1, v1, v34, vcc
	v_rsq_f32_e32 v1, v1
	v_lshl_add_u64 v[34:35], s[46:47], 0, v[52:53]
	v_lshl_add_u64 v[34:35], v[34:35], 0, v[130:131]
	v_mul_f32_e32 v38, 0x45800000, v1
	v_cndmask_b32_e32 v38, v1, v38, vcc
	v_pk_mul_f32 v[32:33], v[32:33], v[38:39] op_sel_hi:[1,0]
	v_pk_mul_f32 v[30:31], v[30:31], v[38:39] op_sel_hi:[1,0]
	v_pk_mul_f32 v[28:29], v[28:29], v[38:39] op_sel_hi:[1,0]
	v_pk_mul_f32 v[26:27], v[26:27], v[38:39] op_sel_hi:[1,0]
	v_pk_mul_f32 v[24:25], v[24:25], v[38:39] op_sel_hi:[1,0]
	v_pk_mul_f32 v[22:23], v[22:23], v[38:39] op_sel_hi:[1,0]
	v_pk_mul_f32 v[40:41], v[20:21], v[38:39] op_sel_hi:[1,0]
	v_pk_mul_f32 v[38:39], v[18:19], v[38:39] op_sel_hi:[1,0]
	v_cvt_pk_bf16_f32 v18, v30, v31
	v_cvt_pk_bf16_f32 v19, v32, v33
	v_cvt_pk_bf16_f32 v20, v26, v27
	v_cvt_pk_bf16_f32 v21, v28, v29
	v_cvt_pk_bf16_f32 v22, v22, v23
	v_cvt_pk_bf16_f32 v23, v24, v25
	v_cvt_pk_bf16_f32 v24, v38, v39
	v_cvt_pk_bf16_f32 v25, v40, v41
	global_store_dwordx4 v[34:35], v[18:21], off
	global_store_dwordx4 v[34:35], v[22:25], off offset:256
	s_nop 0
	s_waitcnt vmcnt(10)
	v_mov_b32_e32 v18, v176
	v_mov_b32_e32 v19, v177
	v_mov_b32_e32 v20, v178
	v_mov_b32_e32 v21, v179
	v_mov_b32_e32 v22, v180
	v_mov_b32_e32 v23, v181
	v_mov_b32_e32 v24, v182
	v_mov_b32_e32 v25, v183
	v_mov_b32_e32 v26, v184
	v_mov_b32_e32 v27, v185
	v_mov_b32_e32 v28, v186
	v_mov_b32_e32 v29, v187
	v_mov_b32_e32 v30, v188
	v_mov_b32_e32 v31, v189
	v_mov_b32_e32 v32, v190
	v_mov_b32_e32 v33, v191
	v_mov_b32_e32 v34, v18
	v_mov_b32_e32 v35, v22
	v_mov_b32_e32 v22, v19
	v_mov_b32_e32 v18, v20
	v_mov_b32_e32 v19, v24
	v_mov_b32_e32 v24, v21
	v_mov_b32_e32 v20, v26
	v_mov_b32_e32 v21, v30
	v_mov_b32_e32 v30, v27
	v_mov_b32_e32 v26, v28
	v_mov_b32_e32 v27, v32
	v_mov_b32_e32 v32, v29
	v_pk_add_f32 v[22:23], v[34:35], v[22:23]
	v_pk_add_f32 v[18:19], v[18:19], v[24:25]
	v_pk_add_f32 v[20:21], v[20:21], v[30:31]
	v_pk_add_f32 v[24:25], v[26:27], v[32:33]
	v_pk_add_f32 v[18:19], v[22:23], v[18:19]
	v_pk_add_f32 v[20:21], v[20:21], v[24:25]
	s_nop 0
	v_pk_add_f32 v[18:19], v[18:19], v[20:21]
	s_nop 0
	v_add_f32_e32 v1, v18, v19
	v_fmac_f32_e32 v134, 0x3a800000, v1
	v_mul_f32_e32 v1, 0x4b800000, v134
	v_cmp_gt_f32_e32 vcc, s6, v134
	v_lshlrev_b64 v[18:19], 11, v[50:51]
	v_lshl_add_u64 v[18:19], s[46:47], 0, v[18:19]
	v_cndmask_b32_e32 v1, v134, v1, vcc
	v_rsq_f32_e32 v1, v1
	v_lshl_add_u64 v[18:19], v[18:19], 0, v[130:131]
	v_mul_f32_e32 v20, 0x45800000, v1
	v_cndmask_b32_e32 v20, v1, v20, vcc
	v_pk_mul_f32 v[16:17], v[16:17], v[20:21] op_sel_hi:[1,0]
	v_pk_mul_f32 v[14:15], v[14:15], v[20:21] op_sel_hi:[1,0]
	v_pk_mul_f32 v[12:13], v[12:13], v[20:21] op_sel_hi:[1,0]
	v_pk_mul_f32 v[10:11], v[10:11], v[20:21] op_sel_hi:[1,0]
	v_pk_mul_f32 v[8:9], v[8:9], v[20:21] op_sel_hi:[1,0]
	v_pk_mul_f32 v[6:7], v[6:7], v[20:21] op_sel_hi:[1,0]
	v_pk_mul_f32 v[22:23], v[4:5], v[20:21] op_sel_hi:[1,0]
	v_pk_mul_f32 v[20:21], v[2:3], v[20:21] op_sel_hi:[1,0]
	v_cvt_pk_bf16_f32 v2, v14, v15
	v_cvt_pk_bf16_f32 v3, v16, v17
	v_cvt_pk_bf16_f32 v4, v10, v11
	v_cvt_pk_bf16_f32 v5, v12, v13
	v_cvt_pk_bf16_f32 v6, v6, v7
	v_cvt_pk_bf16_f32 v7, v8, v9
	v_cvt_pk_bf16_f32 v8, v20, v21
	v_cvt_pk_bf16_f32 v9, v22, v23
	global_store_dwordx4 v[18:19], v[2:5], off
	global_store_dwordx4 v[18:19], v[6:9], off offset:256
	s_waitcnt vmcnt(0)
	s_cbranch_scc0 .LBB0_857
	s_barrier

.LBB0_2059:
	s_lshl_b32 s20, s33, 8
	v_mov_b32_e32 v142, v146
	v_mov_b32_e32 v164, v1
	s_add_i32 s20, s20, s41
	v_xor_b32_e32 v165, 32, v151
	v_add_u32_e32 v144, s20, v142
	s_lshl_b32 s20, s12, 8
	s_or_b32 s20, s20, s42
	v_ashrrev_i32_e32 v145, 31, v144
	v_lshl_add_u32 v142, v164, 2, s20
	v_lshlrev_b64 v[152:153], 11, v[144:145]
	v_ashrrev_i32_e32 v143, 31, v142
	v_lshl_add_u64 v[152:153], s[84:85], 0, v[152:153]
	v_lshl_add_u64 v[154:155], v[142:143], 1, v[152:153]
	global_load_dwordx2 v[156:157], v[154:155], off
	global_load_dwordx2 v[158:159], v[154:155], off offset:32
	global_load_dwordx2 v[160:161], v[154:155], off offset:256
	global_load_dwordx2 v[162:163], v[154:155], off offset:288
	v_add_co_u32_e32 v228, vcc, 0x8000, v154
	s_nop 1
	v_addc_co_u32_e32 v229, vcc, 0, v155, vcc
	global_load_dwordx2 v[172:173], v[228:229], off
	global_load_dwordx2 v[174:175], v[228:229], off offset:32
	global_load_dwordx2 v[176:177], v[228:229], off offset:256
	global_load_dwordx2 v[178:179], v[228:229], off offset:288
	v_add_co_u32_e32 v228, vcc, 0x10000, v154
	s_nop 1
	v_addc_co_u32_e32 v229, vcc, 0, v155, vcc
	global_load_dwordx2 v[180:181], v[228:229], off
	global_load_dwordx2 v[182:183], v[228:229], off offset:32
	global_load_dwordx2 v[184:185], v[228:229], off offset:256
	global_load_dwordx2 v[186:187], v[228:229], off offset:288
	v_add_co_u32_e32 v228, vcc, 0x18000, v154
	s_nop 1
	v_addc_co_u32_e32 v229, vcc, 0, v155, vcc
	global_load_dwordx2 v[188:189], v[228:229], off
	global_load_dwordx2 v[190:191], v[228:229], off offset:32
	global_load_dwordx2 v[192:193], v[228:229], off offset:256
	global_load_dwordx2 v[194:195], v[228:229], off offset:288
	v_add_co_u32_e32 v228, vcc, 0x40000, v154
	s_nop 1
	v_addc_co_u32_e32 v229, vcc, 0, v155, vcc
	global_load_dwordx2 v[196:197], v[228:229], off
	global_load_dwordx2 v[198:199], v[228:229], off offset:32
	global_load_dwordx2 v[200:201], v[228:229], off offset:256
	global_load_dwordx2 v[202:203], v[228:229], off offset:288
	v_add_co_u32_e32 v228, vcc, 0x48000, v154
	s_nop 1
	v_addc_co_u32_e32 v229, vcc, 0, v155, vcc
	global_load_dwordx2 v[204:205], v[228:229], off
	global_load_dwordx2 v[206:207], v[228:229], off offset:32
	global_load_dwordx2 v[208:209], v[228:229], off offset:256
	global_load_dwordx2 v[210:211], v[228:229], off offset:288
	v_add_co_u32_e32 v228, vcc, 0x50000, v154
	s_nop 1
	v_addc_co_u32_e32 v229, vcc, 0, v155, vcc
	global_load_dwordx2 v[212:213], v[228:229], off
	global_load_dwordx2 v[214:215], v[228:229], off offset:32
	global_load_dwordx2 v[216:217], v[228:229], off offset:256
	global_load_dwordx2 v[218:219], v[228:229], off offset:288
	v_add_co_u32_e32 v228, vcc, 0x58000, v154
	s_nop 1
	v_addc_co_u32_e32 v229, vcc, 0, v155, vcc
	global_load_dwordx2 v[220:221], v[228:229], off
	global_load_dwordx2 v[222:223], v[228:229], off offset:32
	global_load_dwordx2 v[224:225], v[228:229], off offset:256
	global_load_dwordx2 v[226:227], v[228:229], off offset:288
	v_and_b32_e32 v153, 64, v151
	v_xor_b32_e32 v152, 16, v151
	v_add_u32_e32 v153, 64, v153
	v_cmp_lt_i32_e32 vcc, v152, v153
	s_lshl_b32 s20, s12, 2
	s_ashr_i32 s21, s20, 31
	v_cndmask_b32_e32 v152, v151, v152, vcc
	v_cmp_lt_i32_e32 vcc, v165, v153
	v_lshlrev_b32_e32 v153, 2, v152
	s_waitcnt vmcnt(28)
	v_lshlrev_b32_e32 v166, 16, v158
	v_cndmask_b32_e32 v165, v151, v165, vcc
	v_cmp_eq_u32_e32 vcc, 0, v164
	v_lshlrev_b32_e32 v152, 2, v165
	v_lshlrev_b32_e32 v164, 16, v156
	v_and_b32_e32 v165, 0xffff0000, v156
	v_lshlrev_b32_e32 v156, 16, v157
	v_and_b32_e32 v157, 0xffff0000, v157
	v_and_b32_e32 v167, 0xffff0000, v158
	v_lshlrev_b32_e32 v158, 16, v159
	v_and_b32_e32 v159, 0xffff0000, v159
	v_lshlrev_b32_e32 v168, 16, v160
	v_and_b32_e32 v169, 0xffff0000, v160
	v_lshlrev_b32_e32 v160, 16, v161
	v_and_b32_e32 v161, 0xffff0000, v161
	v_lshlrev_b32_e32 v170, 16, v162
	v_and_b32_e32 v171, 0xffff0000, v162
	v_pk_add_f32 v[120:121], v[120:121], v[156:157]
	v_pk_add_f32 v[118:119], v[118:119], v[164:165]
	v_pk_add_f32 v[128:129], v[128:129], v[158:159]
	v_pk_add_f32 v[126:127], v[126:127], v[166:167]
	v_lshlrev_b32_e32 v162, 16, v163
	v_and_b32_e32 v163, 0xffff0000, v163
	v_pk_add_f32 v[124:125], v[124:125], v[160:161]
	v_pk_add_f32 v[122:123], v[122:123], v[168:169]
	v_pk_add_f32 v[156:157], v[114:115], v[170:171]
	v_cvt_pk_bf16_f32 v114, v118, v119
	v_cvt_pk_bf16_f32 v115, v120, v121
	v_mul_f32_e32 v119, v119, v119
	v_mul_f32_e32 v121, v121, v121
	v_cvt_pk_bf16_f32 v158, v126, v127
	v_mul_f32_e32 v127, v127, v127
	v_mul_f32_e32 v159, v129, v129
	v_pk_add_f32 v[116:117], v[116:117], v[162:163]
	v_mul_f32_e32 v160, v123, v123
	v_mul_f32_e32 v161, v125, v125
	v_fmac_f32_e32 v119, v118, v118
	v_fmac_f32_e32 v121, v120, v120
	v_fmac_f32_e32 v127, v126, v126
	v_fmac_f32_e32 v159, v128, v128
	v_mul_f32_e32 v162, v157, v157
	v_mul_f32_e32 v163, v117, v117
	global_store_dwordx2 v[154:155], v[114:115], off
	v_fmac_f32_e32 v160, v122, v122
	v_fmac_f32_e32 v161, v124, v124
	v_add_f32_e32 v114, v119, v121
	v_add_f32_e32 v115, v127, v159
	v_fmac_f32_e32 v162, v156, v156
	v_fmac_f32_e32 v163, v116, v116
	v_add_f32_e32 v118, v160, v161
	v_add_f32_e32 v114, v114, v115
	v_add_f32_e32 v114, v114, v118
	v_add_f32_e32 v115, v162, v163
	v_add_f32_e32 v114, v114, v115
	ds_bpermute_b32 v115, v153, v114
	v_cvt_pk_bf16_f32 v118, v122, v123
	v_cvt_pk_bf16_f32 v119, v124, v125
	v_cvt_pk_bf16_f32 v159, v128, v129
	global_store_dwordx2 v[154:155], v[118:119], off offset:256
	s_waitcnt lgkmcnt(0)
	v_add_f32_e32 v114, v114, v115
	ds_bpermute_b32 v115, v152, v114
	v_cvt_pk_bf16_f32 v118, v156, v157
	v_cvt_pk_bf16_f32 v119, v116, v117
	global_store_dwordx2 v[154:155], v[158:159], off offset:32
	global_store_dwordx2 v[154:155], v[118:119], off offset:288
	s_and_saveexec_b64 s[22:23], vcc
	s_cbranch_execz .LBB0_2061
	s_waitcnt lgkmcnt(0)
	v_add_f32_e32 v116, v114, v115
	v_lshlrev_b64 v[114:115], 6, v[144:145]
	v_lshl_add_u64 v[114:115], s[14:15], 0, v[114:115]
	v_lshl_add_u64 v[114:115], s[20:21], 2, v[114:115]
	s_lshl_b32 s12, s39, 2
	v_lshl_add_u64 v[114:115], v[114:115], 0, s[12:13]
	global_store_dword v[114:115], v116, off
.LBB0_2061:
	s_or_b64 exec, exec, s[22:23]
	v_add_u32_e32 v114, 16, v144
	s_waitcnt lgkmcnt(0)
	v_ashrrev_i32_e32 v115, 31, v114
	v_lshlrev_b64 v[116:117], 11, v[114:115]
	v_lshl_add_u64 v[116:117], s[84:85], 0, v[116:117]
	v_lshl_add_u64 v[116:117], v[142:143], 1, v[116:117]
	s_waitcnt vmcnt(32)
	v_lshlrev_b32_e32 v126, 16, v172
	v_and_b32_e32 v127, 0xffff0000, v172
	v_lshlrev_b32_e32 v118, 16, v173
	v_and_b32_e32 v119, 0xffff0000, v173
	s_waitcnt vmcnt(31)
	v_lshlrev_b32_e32 v128, 16, v174
	v_and_b32_e32 v129, 0xffff0000, v174
	v_lshlrev_b32_e32 v120, 16, v175
	v_and_b32_e32 v121, 0xffff0000, v175
	s_waitcnt vmcnt(30)
	v_lshlrev_b32_e32 v154, 16, v176
	v_and_b32_e32 v155, 0xffff0000, v176
	v_lshlrev_b32_e32 v122, 16, v177
	v_and_b32_e32 v123, 0xffff0000, v177
	s_waitcnt vmcnt(29)
	v_lshlrev_b32_e32 v156, 16, v178
	v_and_b32_e32 v157, 0xffff0000, v178
	v_pk_add_f32 v[112:113], v[112:113], v[118:119]
	v_pk_add_f32 v[110:111], v[110:111], v[126:127]
	v_pk_add_f32 v[108:109], v[108:109], v[120:121]
	v_pk_add_f32 v[106:107], v[106:107], v[128:129]
	v_lshlrev_b32_e32 v124, 16, v179
	v_and_b32_e32 v125, 0xffff0000, v179
	v_pk_add_f32 v[104:105], v[104:105], v[122:123]
	v_pk_add_f32 v[102:103], v[102:103], v[154:155]
	v_pk_add_f32 v[118:119], v[98:99], v[156:157]
	v_cvt_pk_bf16_f32 v98, v110, v111
	v_cvt_pk_bf16_f32 v99, v112, v113
	v_mul_f32_e32 v111, v111, v111
	v_mul_f32_e32 v113, v113, v113
	v_cvt_pk_bf16_f32 v120, v106, v107
	v_mul_f32_e32 v107, v107, v107
	v_mul_f32_e32 v121, v109, v109
	v_pk_add_f32 v[100:101], v[100:101], v[124:125]
	v_mul_f32_e32 v122, v103, v103
	v_mul_f32_e32 v123, v105, v105
	v_fmac_f32_e32 v111, v110, v110
	v_fmac_f32_e32 v113, v112, v112
	v_fmac_f32_e32 v107, v106, v106
	v_fmac_f32_e32 v121, v108, v108
	v_mul_f32_e32 v124, v119, v119
	v_mul_f32_e32 v125, v101, v101
	global_store_dwordx2 v[116:117], v[98:99], off
	v_fmac_f32_e32 v122, v102, v102
	v_fmac_f32_e32 v123, v104, v104
	v_add_f32_e32 v98, v111, v113
	v_add_f32_e32 v99, v107, v121
	v_fmac_f32_e32 v124, v118, v118
	v_fmac_f32_e32 v125, v100, v100
	v_add_f32_e32 v106, v122, v123
	v_add_f32_e32 v98, v98, v99
	v_add_f32_e32 v98, v98, v106
	v_add_f32_e32 v99, v124, v125
	v_add_f32_e32 v98, v98, v99
	ds_bpermute_b32 v99, v153, v98
	v_cvt_pk_bf16_f32 v102, v102, v103
	v_cvt_pk_bf16_f32 v103, v104, v105
	v_cvt_pk_bf16_f32 v121, v108, v109
	global_store_dwordx2 v[116:117], v[102:103], off offset:256
	s_waitcnt lgkmcnt(0)
	v_add_f32_e32 v98, v98, v99
	ds_bpermute_b32 v99, v152, v98
	v_cvt_pk_bf16_f32 v102, v118, v119
	v_cvt_pk_bf16_f32 v103, v100, v101
	global_store_dwordx2 v[116:117], v[120:121], off offset:32
	global_store_dwordx2 v[116:117], v[102:103], off offset:288
	s_and_saveexec_b64 s[22:23], vcc
	s_cbranch_execz .LBB0_2063
	s_waitcnt lgkmcnt(0)
	v_add_f32_e32 v100, v98, v99
	v_lshlrev_b64 v[98:99], 6, v[114:115]
	v_lshl_add_u64 v[98:99], s[14:15], 0, v[98:99]
	v_lshl_add_u64 v[98:99], s[20:21], 2, v[98:99]
	s_lshl_b32 s12, s39, 2
	v_lshl_add_u64 v[98:99], v[98:99], 0, s[12:13]
	global_store_dword v[98:99], v100, off
.LBB0_2063:
	s_or_b64 exec, exec, s[22:23]
	v_add_u32_e32 v98, 32, v144
	s_waitcnt lgkmcnt(0)
	v_ashrrev_i32_e32 v99, 31, v98
	v_lshlrev_b64 v[100:101], 11, v[98:99]
	v_lshl_add_u64 v[100:101], s[84:85], 0, v[100:101]
	v_lshl_add_u64 v[100:101], v[142:143], 1, v[100:101]
	s_waitcnt vmcnt(33)
	v_lshlrev_b32_e32 v110, 16, v180
	v_and_b32_e32 v111, 0xffff0000, v180
	v_lshlrev_b32_e32 v102, 16, v181
	v_and_b32_e32 v103, 0xffff0000, v181
	s_waitcnt vmcnt(32)
	v_lshlrev_b32_e32 v112, 16, v182
	v_and_b32_e32 v113, 0xffff0000, v182
	v_lshlrev_b32_e32 v104, 16, v183
	v_and_b32_e32 v105, 0xffff0000, v183
	s_waitcnt vmcnt(31)
	v_lshlrev_b32_e32 v114, 16, v184
	v_and_b32_e32 v115, 0xffff0000, v184
	v_lshlrev_b32_e32 v106, 16, v185
	v_and_b32_e32 v107, 0xffff0000, v185
	s_waitcnt vmcnt(30)
	v_lshlrev_b32_e32 v116, 16, v186
	v_and_b32_e32 v117, 0xffff0000, v186
	v_pk_add_f32 v[96:97], v[96:97], v[102:103]
	v_pk_add_f32 v[94:95], v[94:95], v[110:111]
	v_pk_add_f32 v[92:93], v[92:93], v[104:105]
	v_pk_add_f32 v[90:91], v[90:91], v[112:113]
	v_lshlrev_b32_e32 v108, 16, v187
	v_and_b32_e32 v109, 0xffff0000, v187
	v_pk_add_f32 v[88:89], v[88:89], v[106:107]
	v_pk_add_f32 v[86:87], v[86:87], v[114:115]
	v_pk_add_f32 v[102:103], v[82:83], v[116:117]
	v_cvt_pk_bf16_f32 v82, v94, v95
	v_cvt_pk_bf16_f32 v83, v96, v97
	v_mul_f32_e32 v95, v95, v95
	v_mul_f32_e32 v97, v97, v97
	v_cvt_pk_bf16_f32 v104, v90, v91
	v_mul_f32_e32 v91, v91, v91
	v_mul_f32_e32 v105, v93, v93
	v_pk_add_f32 v[84:85], v[84:85], v[108:109]
	v_mul_f32_e32 v106, v87, v87
	v_mul_f32_e32 v107, v89, v89
	v_fmac_f32_e32 v95, v94, v94
	v_fmac_f32_e32 v97, v96, v96
	v_fmac_f32_e32 v91, v90, v90
	v_fmac_f32_e32 v105, v92, v92
	v_mul_f32_e32 v108, v103, v103
	v_mul_f32_e32 v109, v85, v85
	global_store_dwordx2 v[100:101], v[82:83], off
	v_fmac_f32_e32 v106, v86, v86
	v_fmac_f32_e32 v107, v88, v88
	v_add_f32_e32 v82, v95, v97
	v_add_f32_e32 v83, v91, v105
	v_fmac_f32_e32 v108, v102, v102
	v_fmac_f32_e32 v109, v84, v84
	v_add_f32_e32 v90, v106, v107
	v_add_f32_e32 v82, v82, v83
	v_add_f32_e32 v82, v82, v90
	v_add_f32_e32 v83, v108, v109
	v_add_f32_e32 v82, v82, v83
	ds_bpermute_b32 v83, v153, v82
	v_cvt_pk_bf16_f32 v86, v86, v87
	v_cvt_pk_bf16_f32 v87, v88, v89
	v_cvt_pk_bf16_f32 v105, v92, v93
	global_store_dwordx2 v[100:101], v[86:87], off offset:256
	s_waitcnt lgkmcnt(0)
	v_add_f32_e32 v82, v82, v83
	ds_bpermute_b32 v83, v152, v82
	v_cvt_pk_bf16_f32 v86, v102, v103
	v_cvt_pk_bf16_f32 v87, v84, v85
	global_store_dwordx2 v[100:101], v[104:105], off offset:32
	global_store_dwordx2 v[100:101], v[86:87], off offset:288
	s_and_saveexec_b64 s[22:23], vcc
	s_cbranch_execz .LBB0_2065
	s_waitcnt lgkmcnt(0)
	v_add_f32_e32 v84, v82, v83
	v_lshlrev_b64 v[82:83], 6, v[98:99]
	v_lshl_add_u64 v[82:83], s[14:15], 0, v[82:83]
	v_lshl_add_u64 v[82:83], s[20:21], 2, v[82:83]
	s_lshl_b32 s12, s39, 2
	v_lshl_add_u64 v[82:83], v[82:83], 0, s[12:13]
	global_store_dword v[82:83], v84, off
.LBB0_2065:
	s_or_b64 exec, exec, s[22:23]
	v_add_u32_e32 v82, 48, v144
	s_waitcnt lgkmcnt(0)
	v_ashrrev_i32_e32 v83, 31, v82
	v_lshlrev_b64 v[84:85], 11, v[82:83]
	v_lshl_add_u64 v[84:85], s[84:85], 0, v[84:85]
	v_lshl_add_u64 v[84:85], v[142:143], 1, v[84:85]
	s_waitcnt vmcnt(34)
	v_lshlrev_b32_e32 v94, 16, v188
	v_and_b32_e32 v95, 0xffff0000, v188
	v_lshlrev_b32_e32 v86, 16, v189
	v_and_b32_e32 v87, 0xffff0000, v189
	s_waitcnt vmcnt(33)
	v_lshlrev_b32_e32 v96, 16, v190
	v_and_b32_e32 v97, 0xffff0000, v190
	v_lshlrev_b32_e32 v88, 16, v191
	v_and_b32_e32 v89, 0xffff0000, v191
	s_waitcnt vmcnt(32)
	v_lshlrev_b32_e32 v98, 16, v192
	v_and_b32_e32 v99, 0xffff0000, v192
	v_lshlrev_b32_e32 v90, 16, v193
	v_and_b32_e32 v91, 0xffff0000, v193
	s_waitcnt vmcnt(31)
	v_lshlrev_b32_e32 v100, 16, v194
	v_and_b32_e32 v101, 0xffff0000, v194
	v_pk_add_f32 v[80:81], v[80:81], v[86:87]
	v_pk_add_f32 v[78:79], v[78:79], v[94:95]
	v_pk_add_f32 v[76:77], v[76:77], v[88:89]
	v_pk_add_f32 v[74:75], v[74:75], v[96:97]
	v_lshlrev_b32_e32 v92, 16, v195
	v_and_b32_e32 v93, 0xffff0000, v195
	v_pk_add_f32 v[72:73], v[72:73], v[90:91]
	v_pk_add_f32 v[70:71], v[70:71], v[98:99]
	v_pk_add_f32 v[86:87], v[66:67], v[100:101]
	v_cvt_pk_bf16_f32 v66, v78, v79
	v_cvt_pk_bf16_f32 v67, v80, v81
	v_mul_f32_e32 v79, v79, v79
	v_mul_f32_e32 v81, v81, v81
	v_cvt_pk_bf16_f32 v88, v74, v75
	v_mul_f32_e32 v75, v75, v75
	v_mul_f32_e32 v89, v77, v77
	v_pk_add_f32 v[68:69], v[68:69], v[92:93]
	v_mul_f32_e32 v90, v71, v71
	v_mul_f32_e32 v91, v73, v73
	v_fmac_f32_e32 v79, v78, v78
	v_fmac_f32_e32 v81, v80, v80
	v_fmac_f32_e32 v75, v74, v74
	v_fmac_f32_e32 v89, v76, v76
	v_mul_f32_e32 v92, v87, v87
	v_mul_f32_e32 v93, v69, v69
	global_store_dwordx2 v[84:85], v[66:67], off
	v_fmac_f32_e32 v90, v70, v70
	v_fmac_f32_e32 v91, v72, v72
	v_add_f32_e32 v66, v79, v81
	v_add_f32_e32 v67, v75, v89
	v_fmac_f32_e32 v92, v86, v86
	v_fmac_f32_e32 v93, v68, v68
	v_add_f32_e32 v74, v90, v91
	v_add_f32_e32 v66, v66, v67
	v_add_f32_e32 v66, v66, v74
	v_add_f32_e32 v67, v92, v93
	v_add_f32_e32 v66, v66, v67
	ds_bpermute_b32 v67, v153, v66
	v_cvt_pk_bf16_f32 v70, v70, v71
	v_cvt_pk_bf16_f32 v71, v72, v73
	v_cvt_pk_bf16_f32 v89, v76, v77
	global_store_dwordx2 v[84:85], v[70:71], off offset:256
	s_waitcnt lgkmcnt(0)
	v_add_f32_e32 v66, v66, v67
	ds_bpermute_b32 v67, v152, v66
	v_cvt_pk_bf16_f32 v70, v86, v87
	v_cvt_pk_bf16_f32 v71, v68, v69
	global_store_dwordx2 v[84:85], v[88:89], off offset:32
	global_store_dwordx2 v[84:85], v[70:71], off offset:288
	s_and_saveexec_b64 s[22:23], vcc
	s_cbranch_execz .LBB0_2067
	s_waitcnt lgkmcnt(0)
	v_add_f32_e32 v68, v66, v67
	v_lshlrev_b64 v[66:67], 6, v[82:83]
	v_lshl_add_u64 v[66:67], s[14:15], 0, v[66:67]
	v_lshl_add_u64 v[66:67], s[20:21], 2, v[66:67]
	s_lshl_b32 s12, s39, 2
	v_lshl_add_u64 v[66:67], v[66:67], 0, s[12:13]
	global_store_dword v[66:67], v68, off
.LBB0_2067:
	s_or_b64 exec, exec, s[22:23]
	v_add_u32_e32 v66, 0x80, v144
	s_waitcnt lgkmcnt(0)
	v_ashrrev_i32_e32 v67, 31, v66
	v_lshlrev_b64 v[68:69], 11, v[66:67]
	v_lshl_add_u64 v[68:69], s[84:85], 0, v[68:69]
	v_lshl_add_u64 v[68:69], v[142:143], 1, v[68:69]
	s_waitcnt vmcnt(35)
	v_lshlrev_b32_e32 v78, 16, v196
	v_and_b32_e32 v79, 0xffff0000, v196
	v_lshlrev_b32_e32 v70, 16, v197
	v_and_b32_e32 v71, 0xffff0000, v197
	s_waitcnt vmcnt(34)
	v_lshlrev_b32_e32 v80, 16, v198
	v_and_b32_e32 v81, 0xffff0000, v198
	v_lshlrev_b32_e32 v72, 16, v199
	v_and_b32_e32 v73, 0xffff0000, v199
	s_waitcnt vmcnt(33)
	v_lshlrev_b32_e32 v82, 16, v200
	v_and_b32_e32 v83, 0xffff0000, v200
	v_lshlrev_b32_e32 v74, 16, v201
	v_and_b32_e32 v75, 0xffff0000, v201
	s_waitcnt vmcnt(32)
	v_lshlrev_b32_e32 v84, 16, v202
	v_and_b32_e32 v85, 0xffff0000, v202
	v_pk_add_f32 v[64:65], v[64:65], v[70:71]
	v_pk_add_f32 v[62:63], v[62:63], v[78:79]
	v_pk_add_f32 v[60:61], v[60:61], v[72:73]
	v_pk_add_f32 v[58:59], v[58:59], v[80:81]
	v_lshlrev_b32_e32 v76, 16, v203
	v_and_b32_e32 v77, 0xffff0000, v203
	v_pk_add_f32 v[56:57], v[56:57], v[74:75]
	v_pk_add_f32 v[54:55], v[54:55], v[82:83]
	v_pk_add_f32 v[70:71], v[50:51], v[84:85]
	v_cvt_pk_bf16_f32 v50, v62, v63
	v_cvt_pk_bf16_f32 v51, v64, v65
	v_mul_f32_e32 v63, v63, v63
	v_mul_f32_e32 v65, v65, v65
	v_cvt_pk_bf16_f32 v72, v58, v59
	v_mul_f32_e32 v59, v59, v59
	v_mul_f32_e32 v73, v61, v61
	v_pk_add_f32 v[52:53], v[52:53], v[76:77]
	v_mul_f32_e32 v74, v55, v55
	v_mul_f32_e32 v75, v57, v57
	v_fmac_f32_e32 v63, v62, v62
	v_fmac_f32_e32 v65, v64, v64
	v_fmac_f32_e32 v59, v58, v58
	v_fmac_f32_e32 v73, v60, v60
	v_mul_f32_e32 v76, v71, v71
	v_mul_f32_e32 v77, v53, v53
	global_store_dwordx2 v[68:69], v[50:51], off
	v_fmac_f32_e32 v74, v54, v54
	v_fmac_f32_e32 v75, v56, v56
	v_add_f32_e32 v50, v63, v65
	v_add_f32_e32 v51, v59, v73
	v_fmac_f32_e32 v76, v70, v70
	v_fmac_f32_e32 v77, v52, v52
	v_add_f32_e32 v58, v74, v75
	v_add_f32_e32 v50, v50, v51
	v_add_f32_e32 v50, v50, v58
	v_add_f32_e32 v51, v76, v77
	v_add_f32_e32 v50, v50, v51
	ds_bpermute_b32 v51, v153, v50
	v_cvt_pk_bf16_f32 v54, v54, v55
	v_cvt_pk_bf16_f32 v55, v56, v57
	v_cvt_pk_bf16_f32 v73, v60, v61
	global_store_dwordx2 v[68:69], v[54:55], off offset:256
	s_waitcnt lgkmcnt(0)
	v_add_f32_e32 v50, v50, v51
	ds_bpermute_b32 v51, v152, v50
	v_cvt_pk_bf16_f32 v54, v70, v71
	v_cvt_pk_bf16_f32 v55, v52, v53
	global_store_dwordx2 v[68:69], v[72:73], off offset:32
	global_store_dwordx2 v[68:69], v[54:55], off offset:288
	s_and_saveexec_b64 s[22:23], vcc
	s_cbranch_execz .LBB0_2069
	s_waitcnt lgkmcnt(0)
	v_add_f32_e32 v52, v50, v51
	v_lshlrev_b64 v[50:51], 6, v[66:67]
	v_lshl_add_u64 v[50:51], s[14:15], 0, v[50:51]
	v_lshl_add_u64 v[50:51], s[20:21], 2, v[50:51]
	s_lshl_b32 s12, s39, 2
	v_lshl_add_u64 v[50:51], v[50:51], 0, s[12:13]
	global_store_dword v[50:51], v52, off
.LBB0_2069:
	s_or_b64 exec, exec, s[22:23]
	v_add_u32_e32 v50, 0x90, v144
	s_waitcnt lgkmcnt(0)
	v_ashrrev_i32_e32 v51, 31, v50
	v_lshlrev_b64 v[52:53], 11, v[50:51]
	v_lshl_add_u64 v[52:53], s[84:85], 0, v[52:53]
	v_lshl_add_u64 v[52:53], v[142:143], 1, v[52:53]
	s_waitcnt vmcnt(36)
	v_lshlrev_b32_e32 v62, 16, v204
	v_and_b32_e32 v63, 0xffff0000, v204
	v_lshlrev_b32_e32 v54, 16, v205
	v_and_b32_e32 v55, 0xffff0000, v205
	s_waitcnt vmcnt(35)
	v_lshlrev_b32_e32 v64, 16, v206
	v_and_b32_e32 v65, 0xffff0000, v206
	v_lshlrev_b32_e32 v56, 16, v207
	v_and_b32_e32 v57, 0xffff0000, v207
	s_waitcnt vmcnt(34)
	v_lshlrev_b32_e32 v66, 16, v208
	v_and_b32_e32 v67, 0xffff0000, v208
	v_lshlrev_b32_e32 v58, 16, v209
	v_and_b32_e32 v59, 0xffff0000, v209
	s_waitcnt vmcnt(33)
	v_lshlrev_b32_e32 v68, 16, v210
	v_and_b32_e32 v69, 0xffff0000, v210
	v_pk_add_f32 v[48:49], v[48:49], v[54:55]
	v_pk_add_f32 v[46:47], v[46:47], v[62:63]
	v_pk_add_f32 v[44:45], v[44:45], v[56:57]
	v_pk_add_f32 v[42:43], v[42:43], v[64:65]
	v_lshlrev_b32_e32 v60, 16, v211
	v_and_b32_e32 v61, 0xffff0000, v211
	v_pk_add_f32 v[40:41], v[40:41], v[58:59]
	v_pk_add_f32 v[38:39], v[38:39], v[66:67]
	v_pk_add_f32 v[54:55], v[34:35], v[68:69]
	v_cvt_pk_bf16_f32 v34, v46, v47
	v_cvt_pk_bf16_f32 v35, v48, v49
	v_mul_f32_e32 v47, v47, v47
	v_mul_f32_e32 v49, v49, v49
	v_cvt_pk_bf16_f32 v56, v42, v43
	v_mul_f32_e32 v43, v43, v43
	v_mul_f32_e32 v57, v45, v45
	v_pk_add_f32 v[36:37], v[36:37], v[60:61]
	v_mul_f32_e32 v58, v39, v39
	v_mul_f32_e32 v59, v41, v41
	v_fmac_f32_e32 v47, v46, v46
	v_fmac_f32_e32 v49, v48, v48
	v_fmac_f32_e32 v43, v42, v42
	v_fmac_f32_e32 v57, v44, v44
	v_mul_f32_e32 v60, v55, v55
	v_mul_f32_e32 v61, v37, v37
	global_store_dwordx2 v[52:53], v[34:35], off
	v_fmac_f32_e32 v58, v38, v38
	v_fmac_f32_e32 v59, v40, v40
	v_add_f32_e32 v34, v47, v49
	v_add_f32_e32 v35, v43, v57
	v_fmac_f32_e32 v60, v54, v54
	v_fmac_f32_e32 v61, v36, v36
	v_add_f32_e32 v42, v58, v59
	v_add_f32_e32 v34, v34, v35
	v_add_f32_e32 v34, v34, v42
	v_add_f32_e32 v35, v60, v61
	v_add_f32_e32 v34, v34, v35
	ds_bpermute_b32 v35, v153, v34
	v_cvt_pk_bf16_f32 v38, v38, v39
	v_cvt_pk_bf16_f32 v39, v40, v41
	v_cvt_pk_bf16_f32 v57, v44, v45
	global_store_dwordx2 v[52:53], v[38:39], off offset:256
	s_waitcnt lgkmcnt(0)
	v_add_f32_e32 v34, v34, v35
	ds_bpermute_b32 v35, v152, v34
	v_cvt_pk_bf16_f32 v38, v54, v55
	v_cvt_pk_bf16_f32 v39, v36, v37
	global_store_dwordx2 v[52:53], v[56:57], off offset:32
	global_store_dwordx2 v[52:53], v[38:39], off offset:288
	s_and_saveexec_b64 s[22:23], vcc
	s_cbranch_execz .LBB0_2071
	s_waitcnt lgkmcnt(0)
	v_add_f32_e32 v36, v34, v35
	v_lshlrev_b64 v[34:35], 6, v[50:51]
	v_lshl_add_u64 v[34:35], s[14:15], 0, v[34:35]
	v_lshl_add_u64 v[34:35], s[20:21], 2, v[34:35]
	s_lshl_b32 s12, s39, 2
	v_lshl_add_u64 v[34:35], v[34:35], 0, s[12:13]
	global_store_dword v[34:35], v36, off
.LBB0_2071:
	s_or_b64 exec, exec, s[22:23]
	v_add_u32_e32 v34, 0xa0, v144
	s_waitcnt lgkmcnt(0)
	v_ashrrev_i32_e32 v35, 31, v34
	v_lshlrev_b64 v[36:37], 11, v[34:35]
	v_lshl_add_u64 v[36:37], s[84:85], 0, v[36:37]
	v_lshl_add_u64 v[36:37], v[142:143], 1, v[36:37]
	s_waitcnt vmcnt(37)
	v_lshlrev_b32_e32 v46, 16, v212
	v_and_b32_e32 v47, 0xffff0000, v212
	v_lshlrev_b32_e32 v38, 16, v213
	v_and_b32_e32 v39, 0xffff0000, v213
	s_waitcnt vmcnt(36)
	v_lshlrev_b32_e32 v48, 16, v214
	v_and_b32_e32 v49, 0xffff0000, v214
	v_lshlrev_b32_e32 v40, 16, v215
	v_and_b32_e32 v41, 0xffff0000, v215
	s_waitcnt vmcnt(35)
	v_lshlrev_b32_e32 v50, 16, v216
	v_and_b32_e32 v51, 0xffff0000, v216
	v_lshlrev_b32_e32 v42, 16, v217
	v_and_b32_e32 v43, 0xffff0000, v217
	s_waitcnt vmcnt(34)
	v_lshlrev_b32_e32 v52, 16, v218
	v_and_b32_e32 v53, 0xffff0000, v218
	v_pk_add_f32 v[32:33], v[32:33], v[38:39]
	v_pk_add_f32 v[30:31], v[30:31], v[46:47]
	v_pk_add_f32 v[28:29], v[28:29], v[40:41]
	v_pk_add_f32 v[26:27], v[26:27], v[48:49]
	v_lshlrev_b32_e32 v44, 16, v219
	v_and_b32_e32 v45, 0xffff0000, v219
	v_pk_add_f32 v[24:25], v[24:25], v[42:43]
	v_pk_add_f32 v[22:23], v[22:23], v[50:51]
	v_pk_add_f32 v[38:39], v[18:19], v[52:53]
	v_cvt_pk_bf16_f32 v18, v30, v31
	v_cvt_pk_bf16_f32 v19, v32, v33
	v_mul_f32_e32 v31, v31, v31
	v_mul_f32_e32 v33, v33, v33
	v_cvt_pk_bf16_f32 v40, v26, v27
	v_mul_f32_e32 v27, v27, v27
	v_mul_f32_e32 v41, v29, v29
	v_pk_add_f32 v[20:21], v[20:21], v[44:45]
	v_mul_f32_e32 v42, v23, v23
	v_mul_f32_e32 v43, v25, v25
	v_fmac_f32_e32 v31, v30, v30
	v_fmac_f32_e32 v33, v32, v32
	v_fmac_f32_e32 v27, v26, v26
	v_fmac_f32_e32 v41, v28, v28
	v_mul_f32_e32 v44, v39, v39
	v_mul_f32_e32 v45, v21, v21
	global_store_dwordx2 v[36:37], v[18:19], off
	v_fmac_f32_e32 v42, v22, v22
	v_fmac_f32_e32 v43, v24, v24
	v_add_f32_e32 v18, v31, v33
	v_add_f32_e32 v19, v27, v41
	v_fmac_f32_e32 v44, v38, v38
	v_fmac_f32_e32 v45, v20, v20
	v_add_f32_e32 v26, v42, v43
	v_add_f32_e32 v18, v18, v19
	v_add_f32_e32 v18, v18, v26
	v_add_f32_e32 v19, v44, v45
	v_add_f32_e32 v18, v18, v19
	ds_bpermute_b32 v19, v153, v18
	v_cvt_pk_bf16_f32 v22, v22, v23
	v_cvt_pk_bf16_f32 v23, v24, v25
	v_cvt_pk_bf16_f32 v41, v28, v29
	global_store_dwordx2 v[36:37], v[22:23], off offset:256
	s_waitcnt lgkmcnt(0)
	v_add_f32_e32 v18, v18, v19
	ds_bpermute_b32 v19, v152, v18
	v_cvt_pk_bf16_f32 v22, v38, v39
	v_cvt_pk_bf16_f32 v23, v20, v21
	global_store_dwordx2 v[36:37], v[40:41], off offset:32
	global_store_dwordx2 v[36:37], v[22:23], off offset:288
	s_and_saveexec_b64 s[22:23], vcc
	s_cbranch_execz .LBB0_2073
	s_waitcnt lgkmcnt(0)
	v_add_f32_e32 v20, v18, v19
	v_lshlrev_b64 v[18:19], 6, v[34:35]
	v_lshl_add_u64 v[18:19], s[14:15], 0, v[18:19]
	v_lshl_add_u64 v[18:19], s[20:21], 2, v[18:19]
	s_lshl_b32 s12, s39, 2
	v_lshl_add_u64 v[18:19], v[18:19], 0, s[12:13]
	global_store_dword v[18:19], v20, off
.LBB0_2073:
	s_or_b64 exec, exec, s[22:23]
	v_add_u32_e32 v18, 0xb0, v144
	s_waitcnt lgkmcnt(0)
	v_ashrrev_i32_e32 v19, 31, v18
	v_lshlrev_b64 v[20:21], 11, v[18:19]
	v_lshl_add_u64 v[20:21], s[84:85], 0, v[20:21]
	v_lshl_add_u64 v[20:21], v[142:143], 1, v[20:21]
	s_waitcnt vmcnt(38)
	v_lshlrev_b32_e32 v30, 16, v220
	v_and_b32_e32 v31, 0xffff0000, v220
	v_lshlrev_b32_e32 v22, 16, v221
	v_and_b32_e32 v23, 0xffff0000, v221
	s_waitcnt vmcnt(37)
	v_lshlrev_b32_e32 v32, 16, v222
	v_and_b32_e32 v33, 0xffff0000, v222
	v_lshlrev_b32_e32 v24, 16, v223
	v_and_b32_e32 v25, 0xffff0000, v223
	s_waitcnt vmcnt(36)
	v_lshlrev_b32_e32 v34, 16, v224
	v_and_b32_e32 v35, 0xffff0000, v224
	v_lshlrev_b32_e32 v26, 16, v225
	v_and_b32_e32 v27, 0xffff0000, v225
	s_waitcnt vmcnt(35)
	v_lshlrev_b32_e32 v36, 16, v226
	v_and_b32_e32 v37, 0xffff0000, v226
	v_pk_add_f32 v[16:17], v[16:17], v[22:23]
	v_pk_add_f32 v[14:15], v[14:15], v[30:31]
	v_pk_add_f32 v[12:13], v[12:13], v[24:25]
	v_pk_add_f32 v[10:11], v[10:11], v[32:33]
	v_lshlrev_b32_e32 v28, 16, v227
	v_and_b32_e32 v29, 0xffff0000, v227
	v_pk_add_f32 v[8:9], v[8:9], v[26:27]
	v_pk_add_f32 v[6:7], v[6:7], v[34:35]
	v_pk_add_f32 v[22:23], v[2:3], v[36:37]
	v_cvt_pk_bf16_f32 v2, v14, v15
	v_cvt_pk_bf16_f32 v3, v16, v17
	v_mul_f32_e32 v15, v15, v15
	v_mul_f32_e32 v17, v17, v17
	v_cvt_pk_bf16_f32 v24, v10, v11
	v_mul_f32_e32 v11, v11, v11
	v_mul_f32_e32 v25, v13, v13
	v_pk_add_f32 v[4:5], v[4:5], v[28:29]
	v_mul_f32_e32 v26, v7, v7
	v_mul_f32_e32 v27, v9, v9
	v_fmac_f32_e32 v15, v14, v14
	v_fmac_f32_e32 v17, v16, v16
	v_fmac_f32_e32 v11, v10, v10
	v_fmac_f32_e32 v25, v12, v12
	v_mul_f32_e32 v28, v23, v23
	v_mul_f32_e32 v29, v5, v5
	global_store_dwordx2 v[20:21], v[2:3], off
	v_fmac_f32_e32 v26, v6, v6
	v_fmac_f32_e32 v27, v8, v8
	v_add_f32_e32 v2, v15, v17
	v_add_f32_e32 v3, v11, v25
	v_fmac_f32_e32 v28, v22, v22
	v_fmac_f32_e32 v29, v4, v4
	v_add_f32_e32 v10, v26, v27
	v_add_f32_e32 v2, v2, v3
	v_add_f32_e32 v2, v2, v10
	v_add_f32_e32 v3, v28, v29
	v_add_f32_e32 v2, v2, v3
	ds_bpermute_b32 v3, v153, v2
	v_cvt_pk_bf16_f32 v6, v6, v7
	v_cvt_pk_bf16_f32 v7, v8, v9
	v_cvt_pk_bf16_f32 v25, v12, v13
	global_store_dwordx2 v[20:21], v[6:7], off offset:256
	s_waitcnt lgkmcnt(0)
	v_add_f32_e32 v2, v2, v3
	ds_bpermute_b32 v3, v152, v2
	v_cvt_pk_bf16_f32 v6, v22, v23
	v_cvt_pk_bf16_f32 v7, v4, v5
	global_store_dwordx2 v[20:21], v[24:25], off offset:32
	global_store_dwordx2 v[20:21], v[6:7], off offset:288
	s_and_saveexec_b64 s[22:23], vcc
	s_cbranch_execz .LBB0_2045
	s_waitcnt lgkmcnt(0)
	v_add_f32_e32 v4, v2, v3
	v_lshlrev_b64 v[2:3], 6, v[18:19]
	v_lshl_add_u64 v[2:3], s[14:15], 0, v[2:3]
	v_lshl_add_u64 v[2:3], s[20:21], 2, v[2:3]
	s_lshl_b32 s12, s39, 2
	v_lshl_add_u64 v[2:3], v[2:3], 0, s[12:13]
	global_store_dword v[2:3], v4, off
	s_branch .LBB0_2045

.LBB0_2136:
	s_add_u32 s4, s48, 0x18600000
	s_addc_u32 s5, s49, 0
	s_lshl_b32 s6, s20, 8
	s_add_i32 s22, s22, s6
	s_lshl_b32 s7, s19, 8
	v_add_u32_e32 v132, s22, v139
	v_ashrrev_i32_e32 v133, 31, v132
	v_lshlrev_b64 v[134:135], 6, v[132:133]
	v_lshl_add_u64 v[134:135], s[4:5], 0, v[134:135]
	global_load_dwordx4 v[140:143], v[134:135], off
	global_load_dwordx4 v[144:147], v[134:135], off offset:32
	global_load_dwordx4 v[148:151], v[134:135], off offset:16
	global_load_dwordx4 v[152:155], v[134:135], off offset:48
	v_mov_b32_e32 v240, v134
	v_mov_b32_e32 v241, v135
	v_add_co_u32_e32 v242, vcc, 0x400, v240
	s_nop 1
	v_addc_co_u32_e32 v243, vcc, 0, v241, vcc
	global_load_dwordx4 v[160:163], v[242:243], off
	global_load_dwordx4 v[164:167], v[242:243], off offset:32
	global_load_dwordx4 v[168:171], v[242:243], off offset:16
	global_load_dwordx4 v[172:175], v[242:243], off offset:48
	v_add_co_u32_e32 v242, vcc, 0x800, v240
	s_nop 1
	v_addc_co_u32_e32 v243, vcc, 0, v241, vcc
	global_load_dwordx4 v[176:179], v[242:243], off
	global_load_dwordx4 v[180:183], v[242:243], off offset:32
	global_load_dwordx4 v[184:187], v[242:243], off offset:16
	global_load_dwordx4 v[188:191], v[242:243], off offset:48
	v_add_co_u32_e32 v242, vcc, 0xc00, v240
	s_nop 1
	v_addc_co_u32_e32 v243, vcc, 0, v241, vcc
	global_load_dwordx4 v[192:195], v[242:243], off
	global_load_dwordx4 v[196:199], v[242:243], off offset:32
	global_load_dwordx4 v[200:203], v[242:243], off offset:16
	global_load_dwordx4 v[204:207], v[242:243], off offset:48
	v_add_co_u32_e32 v242, vcc, 0x2000, v240
	s_nop 1
	v_addc_co_u32_e32 v243, vcc, 0, v241, vcc
	global_load_dwordx4 v[208:211], v[242:243], off
	global_load_dwordx4 v[212:215], v[242:243], off offset:32
	global_load_dwordx4 v[216:219], v[242:243], off offset:16
	global_load_dwordx4 v[220:223], v[242:243], off offset:48
	v_add_co_u32_e32 v242, vcc, 0x2400, v240
	s_nop 1
	v_addc_co_u32_e32 v243, vcc, 0, v241, vcc
	global_load_dwordx4 v[224:227], v[242:243], off
	global_load_dwordx4 v[228:231], v[242:243], off offset:32
	global_load_dwordx4 v[232:235], v[242:243], off offset:16
	global_load_dwordx4 v[236:239], v[242:243], off offset:48
	s_or_b32 s7, s21, s7
	v_mov_b32_e32 v134, 0x358637bd
	v_lshl_add_u32 v130, v1, 3, s7
	s_mov_b32 s6, 0x800000
	v_lshlrev_b64 v[156:157], 11, v[132:133]
	v_mov_b32_e32 v129, v131
	v_ashrrev_i32_e32 v131, 31, v130
	v_add_u32_e32 v136, 16, v132
	v_lshlrev_b64 v[130:131], 1, v[130:131]
	v_ashrrev_i32_e32 v137, 31, v136
	v_lshl_add_u64 v[156:157], s[56:57], 0, v[156:157]
	s_cmpk_lt_u32 s18, 0x100
	s_waitcnt vmcnt(20)
	v_mov_b32_e32 v158, v140
	v_mov_b32_e32 v159, v144
	v_mov_b32_e32 v144, v141
	v_mov_b32_e32 v140, v142
	v_mov_b32_e32 v141, v146
	v_mov_b32_e32 v146, v143
	v_mov_b32_e32 v142, v148
	v_mov_b32_e32 v143, v152
	v_mov_b32_e32 v152, v149
	v_mov_b32_e32 v148, v150
	v_mov_b32_e32 v149, v154
	v_mov_b32_e32 v154, v151
	v_pk_add_f32 v[144:145], v[158:159], v[144:145]
	v_pk_add_f32 v[140:141], v[140:141], v[146:147]
	v_pk_add_f32 v[142:143], v[142:143], v[152:153]
	v_pk_add_f32 v[146:147], v[148:149], v[154:155]
	v_pk_add_f32 v[140:141], v[144:145], v[140:141]
	v_pk_add_f32 v[142:143], v[142:143], v[146:147]
	s_nop 0
	v_pk_add_f32 v[140:141], v[140:141], v[142:143]
	v_lshl_add_u64 v[142:143], v[156:157], 0, v[130:131]
	v_add_f32_e32 v1, v140, v141
	v_fmamk_f32 v1, v1, 0x3a800000, v134
	v_mul_f32_e32 v133, 0x4b800000, v1
	v_cmp_gt_f32_e32 vcc, s6, v1
	v_lshlrev_b64 v[140:141], 6, v[136:137]
	v_lshl_add_u64 v[140:141], s[4:5], 0, v[140:141]
	v_cndmask_b32_e32 v1, v1, v133, vcc
	v_rsq_f32_e32 v1, v1
	v_lshlrev_b64 v[136:137], 11, v[136:137]
	v_mul_f32_e32 v133, 0x45800000, v1
	v_cndmask_b32_e32 v144, v1, v133, vcc
	v_pk_mul_f32 v[128:129], v[128:129], v[144:145] op_sel_hi:[1,0]
	v_pk_mul_f32 v[126:127], v[126:127], v[144:145] op_sel_hi:[1,0]
	v_pk_mul_f32 v[124:125], v[124:125], v[144:145] op_sel_hi:[1,0]
	v_pk_mul_f32 v[122:123], v[122:123], v[144:145] op_sel_hi:[1,0]
	v_pk_mul_f32 v[120:121], v[120:121], v[144:145] op_sel_hi:[1,0]
	v_pk_mul_f32 v[118:119], v[118:119], v[144:145] op_sel_hi:[1,0]
	v_pk_mul_f32 v[146:147], v[116:117], v[144:145] op_sel_hi:[1,0]
	v_pk_mul_f32 v[144:145], v[114:115], v[144:145] op_sel_hi:[1,0]
	v_cvt_pk_bf16_f32 v114, v126, v127
	v_cvt_pk_bf16_f32 v115, v128, v129
	v_cvt_pk_bf16_f32 v116, v122, v123
	v_cvt_pk_bf16_f32 v117, v124, v125
	v_cvt_pk_bf16_f32 v118, v118, v119
	v_cvt_pk_bf16_f32 v119, v120, v121
	v_cvt_pk_bf16_f32 v120, v144, v145
	v_cvt_pk_bf16_f32 v121, v146, v147
	global_store_dwordx4 v[142:143], v[114:117], off
	global_store_dwordx4 v[142:143], v[118:121], off offset:256
	s_nop 0
	v_add_u32_e32 v140, 32, v132
	v_ashrrev_i32_e32 v141, 31, v140
	v_lshlrev_b64 v[142:143], 6, v[140:141]
	s_waitcnt vmcnt(18)
	v_mov_b32_e32 v114, v160
	v_mov_b32_e32 v115, v161
	v_mov_b32_e32 v116, v162
	v_mov_b32_e32 v117, v163
	v_mov_b32_e32 v118, v164
	v_mov_b32_e32 v119, v165
	v_mov_b32_e32 v120, v166
	v_mov_b32_e32 v121, v167
	v_mov_b32_e32 v122, v168
	v_mov_b32_e32 v123, v169
	v_mov_b32_e32 v124, v170
	v_mov_b32_e32 v125, v171
	v_mov_b32_e32 v126, v172
	v_mov_b32_e32 v127, v173
	v_mov_b32_e32 v128, v174
	v_mov_b32_e32 v129, v175
	v_add_co_u32_e32 v242, vcc, 0x2800, v240
	s_nop 1
	v_addc_co_u32_e32 v243, vcc, 0, v241, vcc
	global_load_dwordx4 v[160:163], v[242:243], off
	global_load_dwordx4 v[164:167], v[242:243], off offset:32
	global_load_dwordx4 v[168:171], v[242:243], off offset:16
	global_load_dwordx4 v[172:175], v[242:243], off offset:48
	v_mov_b32_e32 v144, v114
	v_mov_b32_e32 v145, v118
	v_mov_b32_e32 v118, v115
	v_mov_b32_e32 v114, v116
	v_mov_b32_e32 v115, v120
	v_mov_b32_e32 v120, v117
	v_mov_b32_e32 v116, v122
	v_mov_b32_e32 v117, v126
	v_mov_b32_e32 v126, v123
	v_mov_b32_e32 v122, v124
	v_mov_b32_e32 v123, v128
	v_mov_b32_e32 v128, v125
	v_pk_add_f32 v[118:119], v[144:145], v[118:119]
	v_pk_add_f32 v[114:115], v[114:115], v[120:121]
	v_pk_add_f32 v[116:117], v[116:117], v[126:127]
	v_pk_add_f32 v[120:121], v[122:123], v[128:129]
	v_pk_add_f32 v[114:115], v[118:119], v[114:115]
	v_pk_add_f32 v[116:117], v[116:117], v[120:121]
	s_nop 0
	v_pk_add_f32 v[114:115], v[114:115], v[116:117]
	v_lshl_add_u64 v[116:117], s[4:5], 0, v[142:143]
	v_add_f32_e32 v1, v114, v115
	v_fmamk_f32 v1, v1, 0x3a800000, v134
	v_mul_f32_e32 v114, 0x4b800000, v1
	v_cmp_gt_f32_e32 vcc, s6, v1
	s_nop 1
	v_cndmask_b32_e32 v1, v1, v114, vcc
	v_rsq_f32_e32 v1, v1
	v_lshl_add_u64 v[114:115], s[56:57], 0, v[136:137]
	v_lshl_add_u64 v[114:115], v[114:115], 0, v[130:131]
	v_mul_f32_e32 v118, 0x45800000, v1
	v_cndmask_b32_e32 v118, v1, v118, vcc
	v_pk_mul_f32 v[112:113], v[112:113], v[118:119] op_sel_hi:[1,0]
	v_pk_mul_f32 v[110:111], v[110:111], v[118:119] op_sel_hi:[1,0]
	v_pk_mul_f32 v[108:109], v[108:109], v[118:119] op_sel_hi:[1,0]
	v_pk_mul_f32 v[106:107], v[106:107], v[118:119] op_sel_hi:[1,0]
	v_pk_mul_f32 v[104:105], v[104:105], v[118:119] op_sel_hi:[1,0]
	v_pk_mul_f32 v[102:103], v[102:103], v[118:119] op_sel_hi:[1,0]
	v_pk_mul_f32 v[120:121], v[100:101], v[118:119] op_sel_hi:[1,0]
	v_pk_mul_f32 v[118:119], v[98:99], v[118:119] op_sel_hi:[1,0]
	v_cvt_pk_bf16_f32 v98, v110, v111
	v_cvt_pk_bf16_f32 v99, v112, v113
	v_cvt_pk_bf16_f32 v100, v106, v107
	v_cvt_pk_bf16_f32 v101, v108, v109
	v_cvt_pk_bf16_f32 v102, v102, v103
	v_cvt_pk_bf16_f32 v103, v104, v105
	v_cvt_pk_bf16_f32 v104, v118, v119
	v_cvt_pk_bf16_f32 v105, v120, v121
	global_store_dwordx4 v[114:115], v[98:101], off
	global_store_dwordx4 v[114:115], v[102:105], off offset:256
	s_nop 0
	v_add_u32_e32 v114, 48, v132
	v_lshlrev_b64 v[116:117], 11, v[140:141]
	v_ashrrev_i32_e32 v115, 31, v114
	v_lshlrev_b64 v[118:119], 6, v[114:115]
	s_waitcnt vmcnt(20)
	v_mov_b32_e32 v98, v176
	v_mov_b32_e32 v99, v177
	v_mov_b32_e32 v100, v178
	v_mov_b32_e32 v101, v179
	v_mov_b32_e32 v102, v180
	v_mov_b32_e32 v103, v181
	v_mov_b32_e32 v104, v182
	v_mov_b32_e32 v105, v183
	v_mov_b32_e32 v106, v184
	v_mov_b32_e32 v107, v185
	v_mov_b32_e32 v108, v186
	v_mov_b32_e32 v109, v187
	v_mov_b32_e32 v110, v188
	v_mov_b32_e32 v111, v189
	v_mov_b32_e32 v112, v190
	v_mov_b32_e32 v113, v191
	v_add_co_u32_e32 v242, vcc, 0x2c00, v240
	s_nop 1
	v_addc_co_u32_e32 v243, vcc, 0, v241, vcc
	global_load_dwordx4 v[176:179], v[242:243], off
	global_load_dwordx4 v[180:183], v[242:243], off offset:32
	global_load_dwordx4 v[184:187], v[242:243], off offset:16
	global_load_dwordx4 v[188:191], v[242:243], off offset:48
	v_mov_b32_e32 v120, v98
	v_mov_b32_e32 v121, v102
	v_mov_b32_e32 v102, v99
	v_mov_b32_e32 v98, v100
	v_mov_b32_e32 v99, v104
	v_mov_b32_e32 v104, v101
	v_mov_b32_e32 v100, v106
	v_mov_b32_e32 v101, v110
	v_mov_b32_e32 v110, v107
	v_mov_b32_e32 v106, v108
	v_mov_b32_e32 v107, v112
	v_mov_b32_e32 v112, v109
	v_pk_add_f32 v[102:103], v[120:121], v[102:103]
	v_pk_add_f32 v[98:99], v[98:99], v[104:105]
	v_pk_add_f32 v[100:101], v[100:101], v[110:111]
	v_pk_add_f32 v[104:105], v[106:107], v[112:113]
	v_pk_add_f32 v[98:99], v[102:103], v[98:99]
	v_pk_add_f32 v[100:101], v[100:101], v[104:105]
	s_nop 0
	v_pk_add_f32 v[98:99], v[98:99], v[100:101]
	v_lshl_add_u64 v[100:101], s[4:5], 0, v[118:119]
	v_add_f32_e32 v1, v98, v99
	v_fmamk_f32 v1, v1, 0x3a800000, v134
	v_mul_f32_e32 v98, 0x4b800000, v1
	v_cmp_gt_f32_e32 vcc, s6, v1
	s_nop 1
	v_cndmask_b32_e32 v1, v1, v98, vcc
	v_rsq_f32_e32 v1, v1
	v_lshl_add_u64 v[98:99], s[56:57], 0, v[116:117]
	v_lshl_add_u64 v[98:99], v[98:99], 0, v[130:131]
	v_mul_f32_e32 v102, 0x45800000, v1
	v_cndmask_b32_e32 v102, v1, v102, vcc
	v_pk_mul_f32 v[96:97], v[96:97], v[102:103] op_sel_hi:[1,0]
	v_pk_mul_f32 v[94:95], v[94:95], v[102:103] op_sel_hi:[1,0]
	v_pk_mul_f32 v[92:93], v[92:93], v[102:103] op_sel_hi:[1,0]
	v_pk_mul_f32 v[90:91], v[90:91], v[102:103] op_sel_hi:[1,0]
	v_pk_mul_f32 v[88:89], v[88:89], v[102:103] op_sel_hi:[1,0]
	v_pk_mul_f32 v[86:87], v[86:87], v[102:103] op_sel_hi:[1,0]
	v_pk_mul_f32 v[104:105], v[84:85], v[102:103] op_sel_hi:[1,0]
	v_pk_mul_f32 v[102:103], v[82:83], v[102:103] op_sel_hi:[1,0]
	v_cvt_pk_bf16_f32 v82, v94, v95
	v_cvt_pk_bf16_f32 v83, v96, v97
	v_cvt_pk_bf16_f32 v84, v90, v91
	v_cvt_pk_bf16_f32 v85, v92, v93
	v_cvt_pk_bf16_f32 v86, v86, v87
	v_cvt_pk_bf16_f32 v87, v88, v89
	v_cvt_pk_bf16_f32 v88, v102, v103
	v_cvt_pk_bf16_f32 v89, v104, v105
	global_store_dwordx4 v[98:99], v[82:85], off
	global_store_dwordx4 v[98:99], v[86:89], off offset:256
	s_nop 0
	v_add_u32_e32 v98, 0x80, v132
	v_lshlrev_b64 v[100:101], 11, v[114:115]
	v_ashrrev_i32_e32 v99, 31, v98
	v_lshlrev_b64 v[102:103], 6, v[98:99]
	s_waitcnt vmcnt(22)
	v_mov_b32_e32 v82, v192
	v_mov_b32_e32 v83, v193
	v_mov_b32_e32 v84, v194
	v_mov_b32_e32 v85, v195
	v_mov_b32_e32 v86, v196
	v_mov_b32_e32 v87, v197
	v_mov_b32_e32 v88, v198
	v_mov_b32_e32 v89, v199
	v_mov_b32_e32 v90, v200
	v_mov_b32_e32 v91, v201
	v_mov_b32_e32 v92, v202
	v_mov_b32_e32 v93, v203
	v_mov_b32_e32 v94, v204
	v_mov_b32_e32 v95, v205
	v_mov_b32_e32 v96, v206
	v_mov_b32_e32 v97, v207
	v_mov_b32_e32 v104, v82
	v_mov_b32_e32 v105, v86
	v_mov_b32_e32 v86, v83
	v_mov_b32_e32 v82, v84
	v_mov_b32_e32 v83, v88
	v_mov_b32_e32 v88, v85
	v_mov_b32_e32 v84, v90
	v_mov_b32_e32 v85, v94
	v_mov_b32_e32 v94, v91
	v_mov_b32_e32 v90, v92
	v_mov_b32_e32 v91, v96
	v_mov_b32_e32 v96, v93
	v_pk_add_f32 v[86:87], v[104:105], v[86:87]
	v_pk_add_f32 v[82:83], v[82:83], v[88:89]
	v_pk_add_f32 v[84:85], v[84:85], v[94:95]
	v_pk_add_f32 v[88:89], v[90:91], v[96:97]
	v_pk_add_f32 v[82:83], v[86:87], v[82:83]
	v_pk_add_f32 v[84:85], v[84:85], v[88:89]
	s_nop 0
	v_pk_add_f32 v[82:83], v[82:83], v[84:85]
	v_lshl_add_u64 v[84:85], s[4:5], 0, v[102:103]
	v_add_f32_e32 v1, v82, v83
	v_fmamk_f32 v1, v1, 0x3a800000, v134
	v_mul_f32_e32 v82, 0x4b800000, v1
	v_cmp_gt_f32_e32 vcc, s6, v1
	s_nop 1
	v_cndmask_b32_e32 v1, v1, v82, vcc
	v_rsq_f32_e32 v1, v1
	v_lshl_add_u64 v[82:83], s[56:57], 0, v[100:101]
	v_lshl_add_u64 v[82:83], v[82:83], 0, v[130:131]
	v_mul_f32_e32 v86, 0x45800000, v1
	v_cndmask_b32_e32 v86, v1, v86, vcc
	v_pk_mul_f32 v[80:81], v[80:81], v[86:87] op_sel_hi:[1,0]
	v_pk_mul_f32 v[78:79], v[78:79], v[86:87] op_sel_hi:[1,0]
	v_pk_mul_f32 v[76:77], v[76:77], v[86:87] op_sel_hi:[1,0]
	v_pk_mul_f32 v[74:75], v[74:75], v[86:87] op_sel_hi:[1,0]
	v_pk_mul_f32 v[72:73], v[72:73], v[86:87] op_sel_hi:[1,0]
	v_pk_mul_f32 v[70:71], v[70:71], v[86:87] op_sel_hi:[1,0]
	v_pk_mul_f32 v[88:89], v[68:69], v[86:87] op_sel_hi:[1,0]
	v_pk_mul_f32 v[86:87], v[66:67], v[86:87] op_sel_hi:[1,0]
	v_cvt_pk_bf16_f32 v66, v78, v79
	v_cvt_pk_bf16_f32 v67, v80, v81
	v_cvt_pk_bf16_f32 v68, v74, v75
	v_cvt_pk_bf16_f32 v69, v76, v77
	v_cvt_pk_bf16_f32 v70, v70, v71
	v_cvt_pk_bf16_f32 v71, v72, v73
	v_cvt_pk_bf16_f32 v72, v86, v87
	v_cvt_pk_bf16_f32 v73, v88, v89
	global_store_dwordx4 v[82:83], v[66:69], off
	global_store_dwordx4 v[82:83], v[70:73], off offset:256
	s_nop 0
	v_add_u32_e32 v82, 0x90, v132
	v_lshlrev_b64 v[84:85], 11, v[98:99]
	v_ashrrev_i32_e32 v83, 31, v82
	v_lshlrev_b64 v[86:87], 6, v[82:83]
	s_waitcnt vmcnt(20)
	v_mov_b32_e32 v66, v208
	v_mov_b32_e32 v67, v209
	v_mov_b32_e32 v68, v210
	v_mov_b32_e32 v69, v211
	v_mov_b32_e32 v70, v212
	v_mov_b32_e32 v71, v213
	v_mov_b32_e32 v72, v214
	v_mov_b32_e32 v73, v215
	v_mov_b32_e32 v74, v216
	v_mov_b32_e32 v75, v217
	v_mov_b32_e32 v76, v218
	v_mov_b32_e32 v77, v219
	v_mov_b32_e32 v78, v220
	v_mov_b32_e32 v79, v221
	v_mov_b32_e32 v80, v222
	v_mov_b32_e32 v81, v223
	v_mov_b32_e32 v88, v66
	v_mov_b32_e32 v89, v70
	v_mov_b32_e32 v70, v67
	v_mov_b32_e32 v66, v68
	v_mov_b32_e32 v67, v72
	v_mov_b32_e32 v72, v69
	v_mov_b32_e32 v68, v74
	v_mov_b32_e32 v69, v78
	v_mov_b32_e32 v78, v75
	v_mov_b32_e32 v74, v76
	v_mov_b32_e32 v75, v80
	v_mov_b32_e32 v80, v77
	v_pk_add_f32 v[70:71], v[88:89], v[70:71]
	v_pk_add_f32 v[66:67], v[66:67], v[72:73]
	v_pk_add_f32 v[68:69], v[68:69], v[78:79]
	v_pk_add_f32 v[72:73], v[74:75], v[80:81]
	v_pk_add_f32 v[66:67], v[70:71], v[66:67]
	v_pk_add_f32 v[68:69], v[68:69], v[72:73]
	s_nop 0
	v_pk_add_f32 v[66:67], v[66:67], v[68:69]
	v_lshl_add_u64 v[68:69], s[4:5], 0, v[86:87]
	v_add_f32_e32 v1, v66, v67
	v_fmamk_f32 v1, v1, 0x3a800000, v134
	v_mul_f32_e32 v66, 0x4b800000, v1
	v_cmp_gt_f32_e32 vcc, s6, v1
	s_nop 1
	v_cndmask_b32_e32 v1, v1, v66, vcc
	v_rsq_f32_e32 v1, v1
	v_lshl_add_u64 v[66:67], s[56:57], 0, v[84:85]
	v_lshl_add_u64 v[66:67], v[66:67], 0, v[130:131]
	v_mul_f32_e32 v70, 0x45800000, v1
	v_cndmask_b32_e32 v70, v1, v70, vcc
	v_pk_mul_f32 v[64:65], v[64:65], v[70:71] op_sel_hi:[1,0]
	v_pk_mul_f32 v[62:63], v[62:63], v[70:71] op_sel_hi:[1,0]
	v_pk_mul_f32 v[60:61], v[60:61], v[70:71] op_sel_hi:[1,0]
	v_pk_mul_f32 v[58:59], v[58:59], v[70:71] op_sel_hi:[1,0]
	v_pk_mul_f32 v[56:57], v[56:57], v[70:71] op_sel_hi:[1,0]
	v_pk_mul_f32 v[54:55], v[54:55], v[70:71] op_sel_hi:[1,0]
	v_pk_mul_f32 v[72:73], v[52:53], v[70:71] op_sel_hi:[1,0]
	v_pk_mul_f32 v[70:71], v[50:51], v[70:71] op_sel_hi:[1,0]
	v_cvt_pk_bf16_f32 v50, v62, v63
	v_cvt_pk_bf16_f32 v51, v64, v65
	v_cvt_pk_bf16_f32 v52, v58, v59
	v_cvt_pk_bf16_f32 v53, v60, v61
	v_cvt_pk_bf16_f32 v54, v54, v55
	v_cvt_pk_bf16_f32 v55, v56, v57
	v_cvt_pk_bf16_f32 v56, v70, v71
	v_cvt_pk_bf16_f32 v57, v72, v73
	global_store_dwordx4 v[66:67], v[50:53], off
	global_store_dwordx4 v[66:67], v[54:57], off offset:256
	s_nop 0
	v_add_u32_e32 v66, 0xa0, v132
	v_lshlrev_b64 v[68:69], 11, v[82:83]
	v_ashrrev_i32_e32 v67, 31, v66
	v_lshlrev_b64 v[70:71], 6, v[66:67]
	s_waitcnt vmcnt(18)
	v_mov_b32_e32 v50, v224
	v_mov_b32_e32 v51, v225
	v_mov_b32_e32 v52, v226
	v_mov_b32_e32 v53, v227
	v_mov_b32_e32 v54, v228
	v_mov_b32_e32 v55, v229
	v_mov_b32_e32 v56, v230
	v_mov_b32_e32 v57, v231
	v_mov_b32_e32 v58, v232
	v_mov_b32_e32 v59, v233
	v_mov_b32_e32 v60, v234
	v_mov_b32_e32 v61, v235
	v_mov_b32_e32 v62, v236
	v_mov_b32_e32 v63, v237
	v_mov_b32_e32 v64, v238
	v_mov_b32_e32 v65, v239
	v_mov_b32_e32 v72, v50
	v_mov_b32_e32 v73, v54
	v_mov_b32_e32 v54, v51
	v_mov_b32_e32 v50, v52
	v_mov_b32_e32 v51, v56
	v_mov_b32_e32 v56, v53
	v_mov_b32_e32 v52, v58
	v_mov_b32_e32 v53, v62
	v_mov_b32_e32 v62, v59
	v_mov_b32_e32 v58, v60
	v_mov_b32_e32 v59, v64
	v_mov_b32_e32 v64, v61
	v_pk_add_f32 v[54:55], v[72:73], v[54:55]
	v_pk_add_f32 v[50:51], v[50:51], v[56:57]
	v_pk_add_f32 v[52:53], v[52:53], v[62:63]
	v_pk_add_f32 v[56:57], v[58:59], v[64:65]
	v_pk_add_f32 v[50:51], v[54:55], v[50:51]
	v_pk_add_f32 v[52:53], v[52:53], v[56:57]
	s_nop 0
	v_pk_add_f32 v[50:51], v[50:51], v[52:53]
	v_lshl_add_u64 v[52:53], s[4:5], 0, v[70:71]
	v_add_f32_e32 v1, v50, v51
	v_fmamk_f32 v1, v1, 0x3a800000, v134
	v_mul_f32_e32 v50, 0x4b800000, v1
	v_cmp_gt_f32_e32 vcc, s6, v1
	s_nop 1
	v_cndmask_b32_e32 v1, v1, v50, vcc
	v_rsq_f32_e32 v1, v1
	v_lshl_add_u64 v[50:51], s[56:57], 0, v[68:69]
	v_lshl_add_u64 v[50:51], v[50:51], 0, v[130:131]
	v_mul_f32_e32 v54, 0x45800000, v1
	v_cndmask_b32_e32 v54, v1, v54, vcc
	v_pk_mul_f32 v[48:49], v[48:49], v[54:55] op_sel_hi:[1,0]
	v_pk_mul_f32 v[46:47], v[46:47], v[54:55] op_sel_hi:[1,0]
	v_pk_mul_f32 v[44:45], v[44:45], v[54:55] op_sel_hi:[1,0]
	v_pk_mul_f32 v[42:43], v[42:43], v[54:55] op_sel_hi:[1,0]
	v_pk_mul_f32 v[40:41], v[40:41], v[54:55] op_sel_hi:[1,0]
	v_pk_mul_f32 v[38:39], v[38:39], v[54:55] op_sel_hi:[1,0]
	v_pk_mul_f32 v[56:57], v[36:37], v[54:55] op_sel_hi:[1,0]
	v_pk_mul_f32 v[54:55], v[34:35], v[54:55] op_sel_hi:[1,0]
	v_cvt_pk_bf16_f32 v34, v46, v47
	v_cvt_pk_bf16_f32 v35, v48, v49
	v_cvt_pk_bf16_f32 v36, v42, v43
	v_cvt_pk_bf16_f32 v37, v44, v45
	v_cvt_pk_bf16_f32 v38, v38, v39
	v_cvt_pk_bf16_f32 v39, v40, v41
	v_cvt_pk_bf16_f32 v40, v54, v55
	v_cvt_pk_bf16_f32 v41, v56, v57
	global_store_dwordx4 v[50:51], v[34:37], off
	global_store_dwordx4 v[50:51], v[38:41], off offset:256
	s_nop 0
	v_add_u32_e32 v50, 0xb0, v132
	v_lshlrev_b64 v[52:53], 11, v[66:67]
	v_ashrrev_i32_e32 v51, 31, v50
	v_lshlrev_b64 v[54:55], 6, v[50:51]
	s_waitcnt vmcnt(14)
	v_mov_b32_e32 v34, v160
	v_mov_b32_e32 v35, v161
	v_mov_b32_e32 v36, v162
	v_mov_b32_e32 v37, v163
	v_mov_b32_e32 v38, v164
	v_mov_b32_e32 v39, v165
	v_mov_b32_e32 v40, v166
	v_mov_b32_e32 v41, v167
	v_mov_b32_e32 v42, v168
	v_mov_b32_e32 v43, v169
	v_mov_b32_e32 v44, v170
	v_mov_b32_e32 v45, v171
	v_mov_b32_e32 v46, v172
	v_mov_b32_e32 v47, v173
	v_mov_b32_e32 v48, v174
	v_mov_b32_e32 v49, v175
	v_mov_b32_e32 v56, v34
	v_mov_b32_e32 v57, v38
	v_mov_b32_e32 v38, v35
	v_mov_b32_e32 v34, v36
	v_mov_b32_e32 v35, v40
	v_mov_b32_e32 v40, v37
	v_mov_b32_e32 v36, v42
	v_mov_b32_e32 v37, v46
	v_mov_b32_e32 v46, v43
	v_mov_b32_e32 v42, v44
	v_mov_b32_e32 v43, v48
	v_mov_b32_e32 v48, v45
	v_pk_add_f32 v[38:39], v[56:57], v[38:39]
	v_pk_add_f32 v[34:35], v[34:35], v[40:41]
	v_pk_add_f32 v[36:37], v[36:37], v[46:47]
	v_pk_add_f32 v[40:41], v[42:43], v[48:49]
	v_pk_add_f32 v[34:35], v[38:39], v[34:35]
	v_pk_add_f32 v[36:37], v[36:37], v[40:41]
	s_nop 0
	v_pk_add_f32 v[34:35], v[34:35], v[36:37]
	v_lshl_add_u64 v[36:37], s[4:5], 0, v[54:55]
	v_add_f32_e32 v1, v34, v35
	v_fmamk_f32 v1, v1, 0x3a800000, v134
	v_mul_f32_e32 v34, 0x4b800000, v1
	v_cmp_gt_f32_e32 vcc, s6, v1
	s_nop 1
	v_cndmask_b32_e32 v1, v1, v34, vcc
	v_rsq_f32_e32 v1, v1
	v_lshl_add_u64 v[34:35], s[56:57], 0, v[52:53]
	v_lshl_add_u64 v[34:35], v[34:35], 0, v[130:131]
	v_mul_f32_e32 v38, 0x45800000, v1
	v_cndmask_b32_e32 v38, v1, v38, vcc
	v_pk_mul_f32 v[32:33], v[32:33], v[38:39] op_sel_hi:[1,0]
	v_pk_mul_f32 v[30:31], v[30:31], v[38:39] op_sel_hi:[1,0]
	v_pk_mul_f32 v[28:29], v[28:29], v[38:39] op_sel_hi:[1,0]
	v_pk_mul_f32 v[26:27], v[26:27], v[38:39] op_sel_hi:[1,0]
	v_pk_mul_f32 v[24:25], v[24:25], v[38:39] op_sel_hi:[1,0]
	v_pk_mul_f32 v[22:23], v[22:23], v[38:39] op_sel_hi:[1,0]
	v_pk_mul_f32 v[40:41], v[20:21], v[38:39] op_sel_hi:[1,0]
	v_pk_mul_f32 v[38:39], v[18:19], v[38:39] op_sel_hi:[1,0]
	v_cvt_pk_bf16_f32 v18, v30, v31
	v_cvt_pk_bf16_f32 v19, v32, v33
	v_cvt_pk_bf16_f32 v20, v26, v27
	v_cvt_pk_bf16_f32 v21, v28, v29
	v_cvt_pk_bf16_f32 v22, v22, v23
	v_cvt_pk_bf16_f32 v23, v24, v25
	v_cvt_pk_bf16_f32 v24, v38, v39
	v_cvt_pk_bf16_f32 v25, v40, v41
	global_store_dwordx4 v[34:35], v[18:21], off
	global_store_dwordx4 v[34:35], v[22:25], off offset:256
	s_nop 0
	s_waitcnt vmcnt(10)
	v_mov_b32_e32 v18, v176
	v_mov_b32_e32 v19, v177
	v_mov_b32_e32 v20, v178
	v_mov_b32_e32 v21, v179
	v_mov_b32_e32 v22, v180
	v_mov_b32_e32 v23, v181
	v_mov_b32_e32 v24, v182
	v_mov_b32_e32 v25, v183
	v_mov_b32_e32 v26, v184
	v_mov_b32_e32 v27, v185
	v_mov_b32_e32 v28, v186
	v_mov_b32_e32 v29, v187
	v_mov_b32_e32 v30, v188
	v_mov_b32_e32 v31, v189
	v_mov_b32_e32 v32, v190
	v_mov_b32_e32 v33, v191
	v_mov_b32_e32 v34, v18
	v_mov_b32_e32 v35, v22
	v_mov_b32_e32 v22, v19
	v_mov_b32_e32 v18, v20
	v_mov_b32_e32 v19, v24
	v_mov_b32_e32 v24, v21
	v_mov_b32_e32 v20, v26
	v_mov_b32_e32 v21, v30
	v_mov_b32_e32 v30, v27
	v_mov_b32_e32 v26, v28
	v_mov_b32_e32 v27, v32
	v_mov_b32_e32 v32, v29
	v_pk_add_f32 v[22:23], v[34:35], v[22:23]
	v_pk_add_f32 v[18:19], v[18:19], v[24:25]
	v_pk_add_f32 v[20:21], v[20:21], v[30:31]
	v_pk_add_f32 v[24:25], v[26:27], v[32:33]
	v_pk_add_f32 v[18:19], v[22:23], v[18:19]
	v_pk_add_f32 v[20:21], v[20:21], v[24:25]
	s_nop 0
	v_pk_add_f32 v[18:19], v[18:19], v[20:21]
	s_nop 0
	v_add_f32_e32 v1, v18, v19
	v_fmac_f32_e32 v134, 0x3a800000, v1
	v_mul_f32_e32 v1, 0x4b800000, v134
	v_cmp_gt_f32_e32 vcc, s6, v134
	v_lshlrev_b64 v[18:19], 11, v[50:51]
	v_lshl_add_u64 v[18:19], s[56:57], 0, v[18:19]
	v_cndmask_b32_e32 v1, v134, v1, vcc
	v_rsq_f32_e32 v1, v1
	v_lshl_add_u64 v[18:19], v[18:19], 0, v[130:131]
	v_mul_f32_e32 v20, 0x45800000, v1
	v_cndmask_b32_e32 v20, v1, v20, vcc
	v_pk_mul_f32 v[16:17], v[16:17], v[20:21] op_sel_hi:[1,0]
	v_pk_mul_f32 v[14:15], v[14:15], v[20:21] op_sel_hi:[1,0]
	v_pk_mul_f32 v[12:13], v[12:13], v[20:21] op_sel_hi:[1,0]
	v_pk_mul_f32 v[10:11], v[10:11], v[20:21] op_sel_hi:[1,0]
	v_pk_mul_f32 v[8:9], v[8:9], v[20:21] op_sel_hi:[1,0]
	v_pk_mul_f32 v[6:7], v[6:7], v[20:21] op_sel_hi:[1,0]
	v_pk_mul_f32 v[22:23], v[4:5], v[20:21] op_sel_hi:[1,0]
	v_pk_mul_f32 v[20:21], v[2:3], v[20:21] op_sel_hi:[1,0]
	v_cvt_pk_bf16_f32 v2, v14, v15
	v_cvt_pk_bf16_f32 v3, v16, v17
	v_cvt_pk_bf16_f32 v4, v10, v11
	v_cvt_pk_bf16_f32 v5, v12, v13
	v_cvt_pk_bf16_f32 v6, v6, v7
	v_cvt_pk_bf16_f32 v7, v8, v9
	v_cvt_pk_bf16_f32 v8, v20, v21
	v_cvt_pk_bf16_f32 v9, v22, v23
	global_store_dwordx4 v[18:19], v[2:5], off
	global_store_dwordx4 v[18:19], v[6:9], off offset:256
	s_waitcnt vmcnt(0)
	s_cbranch_scc0 .LBB0_2138
	s_barrier
